# speedup vs baseline: 1.0254x; 1.0151x over previous
.LBB2_37:
	v_cvt_f32_u32_e32 v1, s26
	s_lshl_b32 s3, s22, 1
	s_sub_i32 s9, 0, s26
	s_sub_i32 s3, s18, s3
	v_rcp_iflag_f32_e32 v1, v1
	s_add_i32 s8, s17, -1
	s_add_i32 s12, s8, s26
	s_ashr_i32 s15, s12, 31
	v_mul_f32_e32 v1, 0x4f7ffffe, v1
	v_cvt_u32_f32_e32 v1, v1
	s_abs_i32 s12, s12
	v_lshrrev_b32_e32 v2, 3, v0
	s_mov_b32 s13, 0
	v_readfirstlane_b32 s18, v1
	s_mul_i32 s9, s9, s18
	s_mul_hi_u32 s9, s18, s9
	s_add_i32 s18, s18, s9
	s_mul_hi_u32 s9, s12, s18
	s_mul_i32 s18, s9, s26
	s_sub_i32 s12, s12, s18
	s_add_i32 s19, s9, 1
	s_sub_i32 s18, s12, s26
	s_cmp_ge_u32 s12, s26
	s_cselect_b32 s9, s19, s9
	s_cselect_b32 s12, s18, s12
	s_add_i32 s18, s9, 1
	s_cmp_ge_u32 s12, s26
	s_cselect_b32 s9, s18, s9
	s_xor_b32 s9, s9, s15
	s_sub_i32 s19, s9, s15
	s_add_i32 s19, s19, 15
	s_and_b32 s20, s19, -16
	s_mul_i32 s22, s20, s2
	s_lshl_b32 s33, s3, 8
	v_add_u32_e32 v5, s22, v2
	s_ashr_i32 s18, s33, 31
	s_add_i32 s21, s16, 0x1fff
	v_min_i32_e32 v10, s8, v5
	s_lshl_b32 s12, s14, 9
	v_or_b32_e32 v6, s33, v2
	v_mov_b32_e32 v7, s18
	v_sub_u32_e32 v11, s21, v10
	v_cmp_gt_i32_e32 vcc, s16, v10
	v_lshl_add_u64 v[6:7], v[6:7], 0, s[12:13]
	s_lshl_b32 s13, s14, 13
	v_cndmask_b32_e32 v10, v11, v10, vcc
	v_add_u32_e32 v10, s13, v10
	v_ashrrev_i32_e32 v11, 31, v10
	s_waitcnt lgkmcnt(0)
	v_lshl_add_u64 v[10:11], v[10:11], 2, s[10:11]
	global_load_dword v16, v[10:11], off
	v_add_u32_e32 v10, 64, v5
	v_min_i32_e32 v10, s8, v10
	v_sub_u32_e32 v11, s21, v10
	v_cmp_gt_i32_e32 vcc, s16, v10
	v_xor_b32_e32 v4, v2, v0
	v_lshlrev_b32_e32 v1, 4, v4
	v_cndmask_b32_e32 v10, v11, v10, vcc
	v_add_u32_e32 v10, s13, v10
	v_ashrrev_i32_e32 v11, 31, v10
	v_lshl_add_u64 v[10:11], v[10:11], 2, s[10:11]
	global_load_dword v17, v[10:11], off
	v_and_b32_e32 v10, 0x70, v1
	v_add_u32_e32 v1, 0x80, v5
	v_min_i32_e32 v1, s8, v1
	v_sub_u32_e32 v5, s21, v1
	v_cmp_gt_i32_e32 vcc, s16, v1
	v_mov_b32_e32 v3, 0
	v_lshlrev_b64 v[6:7], 11, v[6:7]
	v_cndmask_b32_e32 v1, v5, v1, vcc
	v_add_u32_e32 v14, s13, v1
	v_lshl_add_u64 v[8:9], s[6:7], 0, v[6:7]
	v_mov_b32_e32 v11, v3
	v_ashrrev_i32_e32 v15, 31, v14
	v_lshlrev_b32_e32 v1, 4, v0
	v_lshl_add_u64 v[8:9], v[8:9], 0, v[10:11]
	s_mov_b64 s[2:3], 0x20000
	v_or_b32_e32 v6, 0x40000, v6
	v_lshl_add_u64 v[14:15], v[14:15], 2, s[10:11]
	v_add_u32_e32 v187, 0, v1
	v_lshl_add_u64 v[12:13], v[8:9], 0, s[2:3]
	v_lshl_add_u64 v[6:7], s[6:7], 0, v[6:7]
	s_mov_b64 s[2:3], 0x60000
	global_load_dword v5, v[14:15], off
	v_add_u32_e32 v14, 0x4800, v187
	v_lshl_add_u64 v[222:223], v[6:7], 0, v[10:11]
	v_lshl_add_u64 v[6:7], v[8:9], 0, s[2:3]
	v_readfirstlane_b32 s2, v14
	v_add_u32_e32 v14, 0x6800, v187
	s_mov_b32 m0, s2
	v_readfirstlane_b32 s2, v14
	global_load_lds_dwordx4 v[8:9], off
	s_mov_b32 m0, s2
	v_readfirstlane_b32 s23, v0
	global_load_lds_dwordx4 v[12:13], off
	v_add_u32_e32 v12, 0x8800, v187
	s_lshr_b32 s34, s23, 6
	v_readfirstlane_b32 s2, v12
	v_add_u32_e32 v12, 0xa800, v187
	s_mov_b32 m0, s2
	v_readfirstlane_b32 s2, v12
	global_load_lds_dwordx4 v[222:223], off
	s_mov_b32 m0, s2
	s_add_i32 s2, 0, 0x11000
	v_add_u32_e32 v189, s2, v1
	s_mov_b64 s[2:3], 0x80
	v_readfirstlane_b32 s8, v189
	global_load_lds_dwordx4 v[6:7], off
	v_lshl_add_u64 v[6:7], v[8:9], 0, s[2:3]
	s_mov_b32 m0, s8
	s_mov_b64 s[8:9], 0x20080
	v_add_u32_e32 v12, 0x2000, v189
	global_load_lds_dwordx4 v[6:7], off
	v_lshl_add_u64 v[6:7], v[8:9], 0, s[8:9]
	v_readfirstlane_b32 s8, v12
	v_add_u32_e32 v12, 0x4000, v189
	s_mov_b32 m0, s8
	v_readfirstlane_b32 s8, v12
	global_load_lds_dwordx4 v[6:7], off
	v_lshl_add_u64 v[6:7], v[222:223], 0, s[2:3]
	s_mov_b32 m0, s8
	s_mov_b64 s[8:9], 0x60080
	global_load_lds_dwordx4 v[6:7], off
	v_lshl_add_u64 v[6:7], v[8:9], 0, s[8:9]
	v_add_u32_e32 v8, 0x6000, v189
	s_waitcnt vmcnt(7)
	s_mov_b64 s[82:83], s[4:5]
	v_lshlrev_b32_e32 v5, 11, v5
	v_readfirstlane_b32 s8, v8
	s_mov_b32 m0, s8
	v_readfirstlane_b32 s8, v187
	global_load_lds_dwordx4 v[6:7], off
	v_lshlrev_b32_e32 v6, 11, v16
	v_and_b32_e32 v6, 0xfff800, v6
	v_mov_b32_e32 v7, v3
	v_lshl_add_u64 v[6:7], s[4:5], 0, v[6:7]
	v_lshl_add_u64 v[224:225], v[6:7], 0, v[10:11]
	v_lshlrev_b32_e32 v6, 11, v17
	v_and_b32_e32 v6, 0xfff800, v6
	v_mov_b32_e32 v7, v3
	v_lshl_add_u64 v[6:7], s[4:5], 0, v[6:7]
	v_lshl_add_u64 v[226:227], v[6:7], 0, v[10:11]
	v_add_u32_e32 v6, 0x2000, v187
	s_mov_b32 m0, s8
	v_readfirstlane_b32 s8, v6
	global_load_lds_dwordx4 v[224:225], off
	s_mov_b32 m0, s8
	s_lshr_b32 s8, s19, 3
	global_load_lds_dwordx4 v[226:227], off
	s_and_b32 s8, s8, 0x1ffffffe
	s_add_i32 s8, s8, -16
	v_and_b32_e32 v6, 0xfff800, v5
	v_mov_b32_e32 v7, v3
	s_cmp_lt_i32 s34, s8
	v_lshl_add_u64 v[6:7], s[4:5], 0, v[6:7]
	s_cselect_b64 s[4:5], -1, 0
	s_cmp_ge_i32 s34, s8
	s_cselect_b64 s[8:9], -1, 0
	v_lshl_add_u64 v[228:229], v[6:7], 0, v[10:11]
	s_and_b64 vcc, exec, s[8:9]
	s_cbranch_vccnz .LBB2_39
	v_add_u32_e32 v5, 0x4000, v187
	s_nop 0
	v_readfirstlane_b32 s14, v5
	s_mov_b32 m0, s14
	s_nop 0
	global_load_lds_dwordx4 v[228:229], off

.LBB2_65:
	s_cmpk_gt_u32 s19, 0x8f
	v_lshrrev_b32_e32 v6, 4, v0
	v_bfe_u32 v191, v0, 4, 2
	s_cselect_b64 s[10:11], -1, 0
	v_and_b32_e32 v7, 7, v0
	s_add_u32 s0, s33, s12
	v_lshlrev_b32_e32 v5, 7, v5
	v_bitop3_b32 v6, v6, v7, 3 bitop3:0x6c
	v_bitop3_b32 v7, v191, v7, 4 bitop3:0x36
	s_addc_u32 s1, s18, 0
	v_lshl_or_b32 v8, s34, 12, v5
	v_lshlrev_b32_e32 v6, 4, v6
	v_lshlrev_b32_e32 v7, 4, v7
	v_lshl_add_u64 v[2:3], s[0:1], 0, v[2:3]
	v_mov_b32_e32 v70, 0
	v_add_u32_e32 v9, 0x4800, v8
	v_or_b32_e32 v193, v6, v5
	v_or_b32_e32 v197, v7, v5
	v_lshlrev_b64 v[2:3], 11, v[2:3]
	v_and_b32_e32 v4, 7, v4
	v_mov_b32_e32 v72, v70
	v_mov_b32_e32 v73, v70
	v_or_b32_e32 v195, v9, v6
	v_or_b32_e32 v5, v8, v6
	v_or_b32_e32 v6, v8, v7
	v_lshl_or_b32 v2, v4, 4, v2
	v_mov_b32_e32 v71, v70
	v_add_u32_e32 v205, 0, v193
	v_add_u32_e32 v207, 0, v197
	v_mov_b64_e32 v[80:81], v[72:73]
	v_or_b32_e32 v199, v9, v7
	s_mov_b64 s[84:85], s[6:7]
	v_lshl_add_u64 v[230:231], s[6:7], 0, v[2:3]
	s_mov_b32 s35, 0
	s_mov_b64 s[6:7], 0
	s_mov_b64 s[12:13], 0x100
	s_add_i32 s36, 0, 0x1d800
	s_waitcnt lgkmcnt(0)
	s_mov_b64 s[14:15], 0x20100
	s_mov_b64 s[16:17], 0x60100
	s_add_i32 s37, 0, 0x19000
	s_add_i32 s38, 0, 0x1d000
	v_add_u32_e32 v201, 0, v5
	v_add_u32_e32 v203, 0, v6
	s_mov_b64 s[18:19], 0x180
	s_mov_b64 s[20:21], 0x20180
	s_mov_b64 s[22:23], 0x60180
	s_mov_b64 s[24:25], 0x200
	s_mov_b64 s[26:27], 0x20200
	s_mov_b64 s[28:29], 0x60200
	s_add_i32 s39, 0, 0x10800
	v_mov_b32_e32 v86, v70
	v_mov_b32_e32 v87, v70
	v_mov_b32_e32 v88, v70
	v_mov_b32_e32 v89, v70
	v_mov_b32_e32 v90, v70
	v_mov_b32_e32 v91, v70
	v_mov_b32_e32 v92, v70
	v_mov_b32_e32 v93, v70
	v_mov_b32_e32 v94, v70
	v_mov_b32_e32 v95, v70
	v_mov_b32_e32 v96, v70
	v_mov_b32_e32 v97, v70
	v_mov_b32_e32 v98, v70
	v_mov_b32_e32 v99, v70
	v_mov_b32_e32 v100, v70
	v_mov_b32_e32 v101, v70
	v_mov_b32_e32 v102, v70
	v_mov_b32_e32 v103, v70
	v_mov_b32_e32 v104, v70
	v_mov_b32_e32 v105, v70
	v_mov_b32_e32 v106, v70
	v_mov_b32_e32 v107, v70
	v_mov_b32_e32 v108, v70
	v_mov_b32_e32 v109, v70
	v_mov_b32_e32 v110, v70
	v_mov_b32_e32 v111, v70
	v_mov_b32_e32 v112, v70
	v_mov_b32_e32 v113, v70
	v_mov_b32_e32 v114, v70
	v_mov_b32_e32 v115, v70
	v_mov_b32_e32 v116, v70
	v_mov_b32_e32 v117, v70
	v_mov_b32_e32 v118, v70
	v_mov_b32_e32 v119, v70
	v_mov_b32_e32 v120, v70
	v_mov_b32_e32 v121, v70
	v_mov_b32_e32 v122, v70
	v_mov_b32_e32 v123, v70
	v_mov_b32_e32 v124, v70
	v_mov_b32_e32 v125, v70
	v_mov_b32_e32 v126, v70
	v_mov_b32_e32 v127, v70
	v_mov_b32_e32 v128, v70
	v_mov_b32_e32 v129, v70
	v_mov_b32_e32 v130, v70
	v_mov_b32_e32 v131, v70
	v_mov_b32_e32 v132, v70
	v_mov_b32_e32 v133, v70
	v_mov_b32_e32 v134, v70
	v_mov_b32_e32 v135, v70
	v_mov_b32_e32 v136, v70
	v_mov_b32_e32 v137, v70
	v_mov_b32_e32 v138, v70
	v_mov_b32_e32 v139, v70
	v_mov_b32_e32 v140, v70
	v_mov_b32_e32 v141, v70
	v_mov_b32_e32 v142, v70
	v_mov_b32_e32 v143, v70
	v_mov_b32_e32 v144, v70
	v_mov_b32_e32 v145, v70
	v_mov_b32_e32 v82, v70
	v_mov_b32_e32 v83, v70
	v_mov_b32_e32 v84, v70
	v_mov_b32_e32 v85, v70
	v_add_u32_e32 v209, 0xc800, v205
	v_add_u32_e32 v211, 0xc800, v207
	v_mov_b64_e32 v[78:79], v[70:71]
	s_lshl_b32 s79, s34, 10
	v_subrev_u32_e32 v252, s84, v230
	v_subrev_u32_e32 v254, s84, v222
	v_add_u32_e32 v253, 0x20000, v252
	v_add_u32_e32 v255, 0x60000, v252
	v_subrev_u32_e32 v224, s82, v224
	v_subrev_u32_e32 v226, s82, v226
	v_subrev_u32_e32 v228, s82, v228
	s_branch .LBB2_68

.LBB2_76:
	s_cmp_gt_u32 s35, 13
	v_lshl_add_u64 v[158:159], v[230:231], 0, s[6:7]
	v_lshl_add_u64 v[160:161], v[222:223], 0, s[6:7]
	v_lshl_add_u64 v[156:157], v[224:225], 0, s[6:7]
	v_lshl_add_u64 v[154:155], v[226:227], 0, s[6:7]
	s_barrier
	s_waitcnt lgkmcnt(0)
	ds_read_b128 v[38:41], v201 offset:18432
	ds_read_b128 v[42:45], v201 offset:20480
	ds_read_b128 v[6:9], v205
	ds_read_b128 v[14:17], v205 offset:2048
	ds_read_b128 v[22:25], v205 offset:4096
	ds_read_b128 v[30:33], v205 offset:6144
	ds_read_b128 v[46:49], v205 offset:8192
	ds_read_b128 v[50:53], v205 offset:10240
	s_cbranch_scc1 .LBB2_79
	s_add_u32 s90, s6, 0x100
	s_addc_u32 s91, s7, 0
	s_add_u32 s86, s84, s90
	s_addc_u32 s87, s85, s91
	s_add_u32 s88, s82, s90
	s_addc_u32 s89, s83, s91
	s_and_b64 vcc, exec, s[2:3]
	s_cbranch_vccnz .Lil_1
	s_add_i32 m0, s79, 0x1d000
	s_nop 0
	global_load_lds_dwordx4 v228, s[88:89]
.Lil_1:
	s_andn2_b64 vcc, exec, s[10:11]
	s_waitcnt lgkmcnt(0)
	v_mfma_f32_16x16x32_f16 v[34:37], v[38:41], v[46:49], v[106:109]
	s_add_i32 m0, s79, 0x1d800
	v_mfma_f32_16x16x32_f16 v[102:105], v[42:45], v[46:49], v[102:105]
	global_load_lds_dwordx4 v252, s[86:87]
	v_mfma_f32_16x16x32_f16 v[98:101], v[38:41], v[50:53], v[98:101]
	s_add_i32 m0, s79, 0x1f800
	v_mfma_f32_16x16x32_f16 v[94:97], v[42:45], v[50:53], v[94:97]
	global_load_lds_dwordx4 v253, s[86:87]
	ds_read_b128 v[46:49], v205 offset:12288
	ds_read_b128 v[50:53], v205 offset:14336
	v_mfma_f32_16x16x32_f16 v[2:5], v[38:41], v[6:9], v[138:141]
	s_add_i32 m0, s79, 0x21800
	v_mfma_f32_16x16x32_f16 v[6:9], v[42:45], v[6:9], v[134:137]
	global_load_lds_dwordx4 v254, s[86:87]
	v_mfma_f32_16x16x32_f16 v[10:13], v[38:41], v[14:17], v[130:133]
	s_add_i32 m0, s79, 0x23800
	v_mfma_f32_16x16x32_f16 v[14:17], v[42:45], v[14:17], v[126:129]
	global_load_lds_dwordx4 v255, s[86:87]
	v_mfma_f32_16x16x32_f16 v[18:21], v[38:41], v[22:25], v[122:125]
	s_add_i32 m0, s79, 0x19000
	v_mfma_f32_16x16x32_f16 v[22:25], v[42:45], v[22:25], v[118:121]
	global_load_lds_dwordx4 v224, s[88:89]
	v_mfma_f32_16x16x32_f16 v[26:29], v[38:41], v[30:33], v[114:117]
	s_add_i32 m0, s79, 0x1b000
	v_mfma_f32_16x16x32_f16 v[30:33], v[42:45], v[30:33], v[110:113]
	global_load_lds_dwordx4 v226, s[88:89]
	s_waitcnt lgkmcnt(0)
	v_mfma_f32_16x16x32_f16 v[90:93], v[38:41], v[46:49], v[90:93]
	v_mfma_f32_16x16x32_f16 v[86:89], v[42:45], v[46:49], v[86:89]
	v_cndmask_b32_e64 v46, 0, 1, s[10:11]
	v_cmp_ne_u32_e64 s[0:1], 1, v46
	v_mfma_f32_16x16x32_f16 v[106:109], v[38:41], v[50:53], v[142:145]
	v_mfma_f32_16x16x32_f16 v[82:85], v[42:45], v[50:53], v[82:85]
	s_cbranch_vccnz .LBB2_81
	s_branch .Lnine_1

.Lnine_1:
	ds_read_b128 v[46:49], v205 offset:16384
	s_waitcnt lgkmcnt(0)
	v_mfma_f32_16x16x32_f16 v[70:73], v[38:41], v[46:49], v[70:73]
	v_mfma_f32_16x16x32_f16 v[78:81], v[42:45], v[46:49], v[78:81]

.LBB2_92:
	s_cmp_gt_u32 s35, 12
	s_barrier
	s_waitcnt lgkmcnt(0)
	v_add_u32_e32 v70, 0, v195
	ds_read_b128 v[146:149], v70 offset:51200
	ds_read_b128 v[150:153], v70 offset:53248
	ds_read_b128 v[70:73], v205 offset:51200
	ds_read_b128 v[78:81], v205 offset:53248
	ds_read_b128 v[232:235], v205 offset:55296
	ds_read_b128 v[236:239], v205 offset:57344
	s_cbranch_scc1 .LBB2_95
	s_add_u32 s90, s6, 0x180
	s_addc_u32 s91, s7, 0
	s_add_u32 s86, s84, s90
	s_addc_u32 s87, s85, s91
	s_add_u32 s88, s82, s90
	s_addc_u32 s89, s83, s91
	s_and_b64 vcc, exec, s[2:3]
	s_cbranch_vccnz .Lil_2
	s_add_i32 m0, s79, 0x4000
	s_nop 0
	global_load_lds_dwordx4 v228, s[88:89]
.Lil_2:
	s_and_b64 vcc, exec, s[0:1]
	s_waitcnt lgkmcnt(2)
	v_mfma_f32_16x16x32_f16 v[82:85], v[146:149], v[70:73], v[74:77]
	s_add_i32 m0, s79, 0x4800
	v_mfma_f32_16x16x32_f16 v[86:89], v[150:153], v[70:73], v[66:69]
	global_load_lds_dwordx4 v252, s[86:87]
	v_mfma_f32_16x16x32_f16 v[90:93], v[146:149], v[78:81], v[62:65]
	s_add_i32 m0, s79, 0x6800
	v_mfma_f32_16x16x32_f16 v[94:97], v[150:153], v[78:81], v[58:61]
	global_load_lds_dwordx4 v253, s[86:87]
	ds_read_b128 v[240:243], v205 offset:59392
	ds_read_b128 v[244:247], v205 offset:61440
	s_waitcnt lgkmcnt(2)
	v_mfma_f32_16x16x32_f16 v[98:101], v[146:149], v[232:235], v[54:57]
	s_add_i32 m0, s79, 0x8800
	v_mfma_f32_16x16x32_f16 v[102:105], v[150:153], v[232:235], v[50:53]
	global_load_lds_dwordx4 v254, s[86:87]
	v_mfma_f32_16x16x32_f16 v[106:109], v[146:149], v[236:239], v[46:49]
	s_add_i32 m0, s79, 0xa800
	v_mfma_f32_16x16x32_f16 v[110:113], v[150:153], v[236:239], v[42:45]
	global_load_lds_dwordx4 v255, s[86:87]
	ds_read_b128 v[232:235], v205 offset:63488
	ds_read_b128 v[236:239], v209 offset:14336
	s_waitcnt lgkmcnt(2)
	v_mfma_f32_16x16x32_f16 v[114:117], v[146:149], v[240:243], v[38:41]
	s_add_i32 m0, s79, 0x0
	v_mfma_f32_16x16x32_f16 v[118:121], v[150:153], v[240:243], v[34:37]
	global_load_lds_dwordx4 v224, s[88:89]
	v_mfma_f32_16x16x32_f16 v[122:125], v[146:149], v[244:247], v[30:33]
	s_add_i32 m0, s79, 0x2000
	v_mfma_f32_16x16x32_f16 v[126:129], v[150:153], v[244:247], v[26:29]
	global_load_lds_dwordx4 v226, s[88:89]
	v_mov_b64_e32 v[80:81], v[4:5]
	v_mov_b64_e32 v[78:79], v[2:3]
	s_waitcnt lgkmcnt(0)
	v_mfma_f32_16x16x32_f16 v[130:133], v[146:149], v[232:235], v[22:25]
	v_mfma_f32_16x16x32_f16 v[134:137], v[150:153], v[232:235], v[18:21]
	v_mov_b64_e32 v[72:73], v[8:9]
	v_mov_b64_e32 v[70:71], v[6:7]
	v_mfma_f32_16x16x32_f16 v[138:141], v[146:149], v[236:239], v[14:17]
	v_mfma_f32_16x16x32_f16 v[142:145], v[150:153], v[236:239], v[10:13]
	s_cbranch_vccnz .LBB2_97
	s_branch .Lnine_2

.Lnine_2:
	ds_read_b128 v[78:81], v209 offset:16384
	s_waitcnt lgkmcnt(0)
	v_mfma_f32_16x16x32_f16 v[70:73], v[146:149], v[78:81], v[6:9]
	v_mfma_f32_16x16x32_f16 v[78:81], v[150:153], v[78:81], v[2:5]

.LBB2_101:
	s_cmp_gt_u32 s35, 11
	s_barrier
	s_waitcnt lgkmcnt(0)
	v_add_u32_e32 v146, s37, v195
	ds_read_b128 v[178:181], v146
	ds_read_b128 v[182:185], v146 offset:2048
	v_add_u32_e32 v213, s37, v193
	ds_read_b128 v[146:149], v213
	ds_read_b128 v[150:153], v213 offset:2048
	ds_read_b128 v[232:235], v213 offset:4096
	ds_read_b128 v[236:239], v213 offset:6144
	ds_read_b128 v[240:243], v213 offset:8192
	ds_read_b128 v[244:247], v213 offset:10240
	s_cbranch_scc1 .LBB2_104
	s_add_u32 s90, s6, 0x200
	s_addc_u32 s91, s7, 0
	s_add_u32 s86, s84, s90
	s_addc_u32 s87, s85, s91
	s_add_u32 s88, s82, s90
	s_addc_u32 s89, s83, s91
	s_and_b64 vcc, exec, s[2:3]
	s_cbranch_vccnz .Lil_3
	s_add_i32 m0, s79, 0x10800
	s_nop 0
	global_load_lds_dwordx4 v228, s[88:89]
.Lil_3:
	s_and_b64 vcc, exec, s[0:1]
	s_waitcnt lgkmcnt(5)
	v_mfma_f32_16x16x32_f16 v[86:89], v[182:185], v[146:149], v[86:89]
	s_add_i32 m0, s79, 0x11000
	v_mfma_f32_16x16x32_f16 v[82:85], v[178:181], v[146:149], v[82:85]
	global_load_lds_dwordx4 v252, s[86:87]
	s_waitcnt lgkmcnt(4)
	v_mfma_f32_16x16x32_f16 v[90:93], v[178:181], v[150:153], v[90:93]
	s_add_i32 m0, s79, 0x13000
	v_mfma_f32_16x16x32_f16 v[94:97], v[182:185], v[150:153], v[94:97]
	global_load_lds_dwordx4 v253, s[86:87]
	s_waitcnt lgkmcnt(2)
	v_mfma_f32_16x16x32_f16 v[106:109], v[178:181], v[236:239], v[106:109]
	s_add_i32 m0, s79, 0x15000
	v_mfma_f32_16x16x32_f16 v[110:113], v[182:185], v[236:239], v[110:113]
	global_load_lds_dwordx4 v254, s[86:87]
	v_mfma_f32_16x16x32_f16 v[98:101], v[178:181], v[232:235], v[98:101]
	s_add_i32 m0, s79, 0x17000
	v_mfma_f32_16x16x32_f16 v[102:105], v[182:185], v[232:235], v[102:105]
	global_load_lds_dwordx4 v255, s[86:87]
	ds_read_b128 v[232:235], v213 offset:12288
	ds_read_b128 v[236:239], v213 offset:14336
	s_waitcnt lgkmcnt(3)
	v_mfma_f32_16x16x32_f16 v[146:149], v[178:181], v[240:243], v[114:117]
	s_add_i32 m0, s79, 0xc800
	v_mfma_f32_16x16x32_f16 v[150:153], v[182:185], v[240:243], v[118:121]
	global_load_lds_dwordx4 v224, s[88:89]
	s_waitcnt lgkmcnt(2)
	v_mfma_f32_16x16x32_f16 v[154:157], v[178:181], v[244:247], v[122:125]
	s_add_i32 m0, s79, 0xe800
	v_mfma_f32_16x16x32_f16 v[158:161], v[182:185], v[244:247], v[126:129]
	global_load_lds_dwordx4 v226, s[88:89]
	s_waitcnt lgkmcnt(1)
	v_mfma_f32_16x16x32_f16 v[162:165], v[178:181], v[232:235], v[130:133]
	v_mfma_f32_16x16x32_f16 v[166:169], v[182:185], v[232:235], v[134:137]
	s_waitcnt lgkmcnt(0)
	v_mfma_f32_16x16x32_f16 v[170:173], v[178:181], v[236:239], v[138:141]
	v_mfma_f32_16x16x32_f16 v[174:177], v[182:185], v[236:239], v[142:145]
	s_cbranch_vccnz .LBB2_106
	s_branch .Lnine_3

.Lnine_3:
	ds_read_b128 v[114:117], v213 offset:16384
	s_waitcnt lgkmcnt(0)
	v_mfma_f32_16x16x32_f16 v[70:73], v[178:181], v[114:117], v[70:73]
	v_mfma_f32_16x16x32_f16 v[78:81], v[182:185], v[114:117], v[78:81]

	.amdhsa_kernel _Z8moe_gemmILi0EEvPKDF16_S1_PvPKyPKiPKfS1_
		.amdhsa_group_segment_fixed_size 0
		.amdhsa_private_segment_fixed_size 0
		.amdhsa_kernarg_size 56
		.amdhsa_user_sgpr_count 2
		.amdhsa_user_sgpr_dispatch_ptr 0
		.amdhsa_user_sgpr_queue_ptr 0
		.amdhsa_user_sgpr_kernarg_segment_ptr 1
		.amdhsa_user_sgpr_dispatch_id 0
		.amdhsa_user_sgpr_kernarg_preload_length 0
		.amdhsa_user_sgpr_kernarg_preload_offset 0
		.amdhsa_user_sgpr_private_segment_size 0
		.amdhsa_uses_dynamic_stack 0
		.amdhsa_enable_private_segment 0
		.amdhsa_system_sgpr_workgroup_id_x 1
		.amdhsa_system_sgpr_workgroup_id_y 0
		.amdhsa_system_sgpr_workgroup_id_z 0
		.amdhsa_system_sgpr_workgroup_info 0
		.amdhsa_system_vgpr_workitem_id 0
		.amdhsa_next_free_vgpr 256
		.amdhsa_next_free_sgpr 92
		.amdhsa_accum_offset 256
		.amdhsa_reserve_vcc 1
		.amdhsa_float_round_mode_32 0
		.amdhsa_float_round_mode_16_64 0
		.amdhsa_float_denorm_mode_32 3
		.amdhsa_float_denorm_mode_16_64 3
		.amdhsa_dx10_clamp 1
		.amdhsa_ieee_mode 1
		.amdhsa_fp16_overflow 0
		.amdhsa_tg_split 0
		.amdhsa_exception_fp_ieee_invalid_op 0
		.amdhsa_exception_fp_denorm_src 0
		.amdhsa_exception_fp_ieee_div_zero 0
		.amdhsa_exception_fp_ieee_overflow 0
		.amdhsa_exception_fp_ieee_underflow 0
		.amdhsa_exception_fp_ieee_inexact 0
		.amdhsa_exception_int_div_zero 0
	.end_amdhsa_kernel

.LBB3_35:
	s_abs_i32 s3, s26
	v_cvt_f32_u32_e32 v1, s3
	s_sub_i32 s11, 0, s3
	s_lshl_b32 s10, s19, 2
	s_add_i32 s15, s12, -1
	v_rcp_iflag_f32_e32 v1, v1
	s_sub_i32 s14, s18, s10
	s_add_i32 s10, s15, s26
	s_xor_b32 s16, s10, s26
	v_mul_f32_e32 v1, 0x4f7ffffe, v1
	v_cvt_u32_f32_e32 v1, v1
	s_abs_i32 s10, s10
	s_ashr_i32 s16, s16, 31
	v_lshlrev_b32_e32 v108, 4, v0
	v_readfirstlane_b32 s17, v1
	s_mul_i32 s11, s11, s17
	s_mul_hi_u32 s11, s17, s11
	s_add_i32 s17, s17, s11
	s_mul_hi_u32 s11, s10, s17
	s_mul_i32 s17, s11, s3
	s_sub_i32 s10, s10, s17
	s_add_i32 s18, s11, 1
	s_sub_i32 s17, s10, s3
	s_cmp_ge_u32 s10, s3
	s_cselect_b32 s11, s18, s11
	s_cselect_b32 s10, s17, s10
	s_add_i32 s17, s11, 1
	s_cmp_ge_u32 s10, s3
	s_cselect_b32 s3, s17, s11
	s_xor_b32 s3, s3, s16
	s_sub_i32 s16, s3, s16
	s_add_i32 s16, s16, 15
	s_and_b32 s17, s16, -16
	v_lshrrev_b32_e32 v1, 3, v0
	s_mul_i32 s19, s17, s2
	v_add_u32_e32 v7, s19, v1
	s_lshl_b32 s2, s13, 13
	s_or_b32 s18, s2, 0x1fff
	v_min_i32_e32 v2, s15, v7
	v_add_u32_e32 v4, 64, v7
	v_sub_u32_e32 v2, s18, v2
	v_min_i32_e32 v4, s15, v4
	v_ashrrev_i32_e32 v3, 31, v2
	v_sub_u32_e32 v4, s18, v4
	s_waitcnt lgkmcnt(0)
	v_lshl_add_u64 v[2:3], v[2:3], 2, s[8:9]
	v_ashrrev_i32_e32 v5, 31, v4
	v_lshl_add_u64 v[4:5], v[4:5], 2, s[8:9]
	global_load_dword v6, v[2:3], off
	global_load_dword v8, v[4:5], off
	v_add_u32_e32 v146, 0x80, v7
	v_min_i32_e32 v146, s15, v146
	v_sub_u32_e32 v146, s18, v146
	v_ashrrev_i32_e32 v147, 31, v146
	v_lshl_add_u64 v[146:147], v[146:147], 2, s[8:9]
	global_load_dword v146, v[146:147], off
	v_add_u32_e32 v109, 0, v108
	s_lshl_b32 s14, s14, 8
	v_add_u32_e32 v4, 0x5000, v109
	v_add_u32_e32 v5, 0x7000, v109
	s_ashr_i32 s30, s14, 31
	s_mov_b32 s11, 0
	v_readfirstlane_b32 s26, v4
	v_readfirstlane_b32 s27, v5
	s_lshl_b32 s10, s13, 10
	v_or_b32_e32 v4, s14, v1
	v_mov_b32_e32 v5, s30
	v_xor_b32_e32 v2, v1, v0
	s_add_i32 s13, 0, 0x12000
	v_lshl_add_u64 v[4:5], v[4:5], 0, s[10:11]
	v_lshlrev_b32_e32 v2, 4, v2
	v_add_u32_e32 v10, 0xb000, v109
	v_add_u32_e32 v110, s13, v108
	v_lshlrev_b64 v[4:5], 10, v[4:5]
	v_mov_b32_e32 v3, 0
	v_and_b32_e32 v2, 0x70, v2
	v_readfirstlane_b32 s29, v10
	v_add_u32_e32 v1, 0x2000, v110
	s_mov_b64 s[66:67], s[6:7]
	v_lshl_add_u64 v[10:11], s[6:7], 0, v[4:5]
	s_mov_b64 s[20:21], 0x10000
	v_add_u32_e32 v9, 0x9000, v109
	v_readfirstlane_b32 s10, v1
	v_or_b32_e32 v4, 0x20000, v4
	v_lshl_add_u64 v[100:101], v[10:11], 0, v[2:3]
	v_add_u32_e32 v1, 0x80, v7
	s_mov_b32 m0, s26
	v_readfirstlane_b32 s28, v9
	v_lshl_add_u64 v[4:5], s[6:7], 0, v[4:5]
	v_lshl_add_u64 v[98:99], v[100:101], 0, s[20:21]
	global_load_lds_dwordx4 v[100:101], off
	v_min_i32_e32 v1, s15, v1
	s_mov_b32 m0, s27
	s_mov_b64 s[22:23], 0x30000
	v_lshl_add_u64 v[96:97], v[4:5], 0, v[2:3]
	global_load_lds_dwordx4 v[98:99], off
	v_sub_u32_e32 v14, s18, v1
	s_mov_b32 m0, s28
	s_mov_b64 s[2:3], 0x80
	v_readfirstlane_b32 s13, v110
	v_lshl_add_u64 v[94:95], v[100:101], 0, s[22:23]
	global_load_lds_dwordx4 v[96:97], off
	v_ashrrev_i32_e32 v15, 31, v14
	s_mov_b32 m0, s29
	s_mov_b64 s[24:25], 0x10080
	v_lshl_add_u64 v[4:5], v[100:101], 0, s[2:3]
	global_load_lds_dwordx4 v[94:95], off
	v_lshl_add_u64 v[14:15], v[14:15], 2, s[8:9]
	s_mov_b32 m0, s13
	v_add_u32_e32 v1, 0x4000, v110
	v_lshl_add_u64 v[10:11], v[100:101], 0, s[24:25]
	global_load_lds_dwordx4 v[4:5], off
	s_mov_b32 m0, s10
	v_readfirstlane_b32 s6, v1
	global_load_lds_dwordx4 v[10:11], off
	s_mov_b32 m0, s6
	s_mov_b64 s[6:7], 0x30080
	v_add_u32_e32 v1, 0x6000, v110
	v_lshl_add_u64 v[12:13], v[96:97], 0, s[2:3]
	v_lshl_add_u64 v[10:11], v[100:101], 0, s[6:7]
	v_readfirstlane_b32 s6, v1
	global_load_lds_dwordx4 v[12:13], off
	s_mov_b32 m0, s6
	v_readfirstlane_b32 s6, v109
	v_add_u32_e32 v1, 0x2000, v109
	global_load_lds_dwordx4 v[10:11], off
	s_waitcnt vmcnt(8)
	s_mov_b64 s[68:69], s[4:5]
	v_mov_b32_e32 v4, v146
	v_ashrrev_i32_e32 v7, 31, v6
	v_lshlrev_b64 v[6:7], 10, v[6:7]
	v_ashrrev_i32_e32 v9, 31, v8
	v_lshl_add_u64 v[6:7], s[4:5], 0, v[6:7]
	v_lshl_add_u64 v[104:105], v[6:7], 0, v[2:3]
	v_lshlrev_b64 v[6:7], 10, v[8:9]
	v_lshl_add_u64 v[6:7], s[4:5], 0, v[6:7]
	s_mov_b32 m0, s6
	v_readfirstlane_b32 s6, v1
	v_lshl_add_u64 v[102:103], v[6:7], 0, v[2:3]
	global_load_lds_dwordx4 v[104:105], off
	s_mov_b32 m0, s6
	s_lshr_b32 s7, s16, 3
	global_load_lds_dwordx4 v[102:103], off
	v_readfirstlane_b32 s6, v0
	s_and_b32 s7, s7, 0x1ffffffe
	s_lshr_b32 s15, s6, 6
	s_add_i32 s7, s7, -16
	s_cmp_lt_i32 s15, s7
	v_ashrrev_i32_e32 v5, 31, v4
	v_lshlrev_b64 v[4:5], 10, v[4:5]
	v_lshl_add_u64 v[4:5], s[4:5], 0, v[4:5]
	s_cselect_b64 s[4:5], -1, 0
	s_cmp_ge_i32 s15, s7
	s_cselect_b64 s[10:11], -1, 0
	v_lshl_add_u64 v[106:107], v[4:5], 0, v[2:3]
	s_and_b64 vcc, exec, s[10:11]
	s_cbranch_vccnz .LBB3_37
	v_add_u32_e32 v1, 0x4000, v109
	s_nop 0
	v_readfirstlane_b32 s7, v1
	s_mov_b32 m0, s7
	s_nop 0
	global_load_lds_dwordx4 v[106:107], off

.LBB3_64:
	s_add_i32 s4, 0, 0x1f000
	v_add_u32_e32 v111, s4, v108
	s_mov_b64 s[6:7], 0x100
	v_readfirstlane_b32 s4, v111
	v_add_u32_e32 v3, 0x2000, v111
	v_lshl_add_u64 v[4:5], v[100:101], 0, s[6:7]
	s_mov_b32 m0, s4
	v_readfirstlane_b32 s4, v3
	v_add_u32_e32 v3, 0x4000, v111
	v_readfirstlane_b32 s70, v0
	s_nop 3
	s_lshr_b32 s70, s70, 6
	s_lshl_b32 s70, s70, 10
	s_add_i32 s76, s70, 0x5000
	s_add_i32 s77, s70, 0x7000
	s_add_i32 s78, s70, 0x9000
	s_add_i32 s79, s70, 0xb000
	s_add_i32 s80, s70, 0x0
	s_add_i32 s81, s70, 0x2000
	s_add_i32 s82, s70, 0x12000
	s_add_i32 s83, s70, 0x14000
	s_add_i32 s84, s70, 0x16000
	s_add_i32 s85, s70, 0x18000
	s_add_i32 s86, s70, 0xd000
	s_add_i32 s87, s70, 0xf000
	s_add_i32 s88, s70, 0x1f000
	s_add_i32 s89, s70, 0x21000
	s_add_i32 s90, s70, 0x23000
	s_add_i32 s91, s70, 0x25000
	s_add_i32 s92, s70, 0x1a000
	s_add_i32 s93, s70, 0x1c000
	v_subrev_u32_e32 v168, s66, v100
	v_subrev_u32_e32 v169, s66, v98
	v_subrev_u32_e32 v170, s66, v96
	v_subrev_u32_e32 v171, s66, v94
	v_subrev_u32_e32 v172, s68, v104
	v_subrev_u32_e32 v173, s68, v102
	s_barrier
	v_lshl_add_u64 v[4:5], v[98:99], 0, s[6:7]
	s_mov_b32 m0, s4
	v_readfirstlane_b32 s4, v3
	v_add_u32_e32 v3, 0x6000, v111
	s_add_i32 s17, 0, 0x1a000
	v_lshl_add_u64 v[4:5], v[96:97], 0, s[6:7]
	s_mov_b32 m0, s4
	v_readfirstlane_b32 s4, v3
	v_add_u32_e32 v112, s17, v108
	v_lshl_add_u64 v[4:5], v[94:95], 0, s[6:7]
	s_mov_b32 m0, s4
	v_readfirstlane_b32 s4, v112
	v_add_u32_e32 v3, 0x2000, v112
	v_lshl_add_u64 v[4:5], v[104:105], 0, s[6:7]
	s_mov_b32 m0, s4
	v_readfirstlane_b32 s4, v3
	v_lshl_add_u64 v[4:5], v[102:103], 0, s[6:7]
	s_mov_b32 m0, s4
	s_and_b64 vcc, exec, s[2:3]
	s_mov_b32 s4, 0
	s_cbranch_vccnz .LBB3_66
	s_add_i32 s5, 0, 0x1e000
	v_add_u32_e32 v3, s5, v108
	v_lshl_add_u64 v[4:5], v[106:107], 0, s[6:7]
	v_readfirstlane_b32 s5, v3
	s_mov_b32 m0, s5
	s_nop 0
	global_load_lds_dwordx4 v[4:5], off
.LBB3_66:
	s_add_u32 s72, s66, 0x100
	s_addc_u32 s73, s67, 0
	s_add_u32 s74, s68, 0x100
	s_addc_u32 s75, s69, 0
	v_lshrrev_b32_e32 v3, 4, v0
	v_and_b32_e32 v62, 7, v0
	v_lshlrev_b32_e32 v115, 7, v2
	s_lshl_b32 s18, s15, 12
	v_bitop3_b32 v2, v3, v62, 3 bitop3:0x6c
	v_lshlrev_b32_e32 v116, 4, v2
	v_or_b32_e32 v63, s18, v115
	v_or_b32_e32 v2, v63, v116
	v_add_u32_e32 v122, 0, v2
	ds_read_b128 v[2:5], v122 offset:20480
	v_or_b32_e32 v113, v116, v115
	v_add_u32_e32 v136, 0, v113
	ds_read_b128 v[6:9], v122 offset:22528
	ds_read_b128 v[10:13], v136
	ds_read_b128 v[14:17], v136 offset:2048
	s_waitcnt lgkmcnt(0)
	v_mfma_f32_16x16x32_f16 v[22:25], v[6:9], v[10:13], 0
	s_mov_b32 s6, s4
	s_mov_b32 s7, s4
	s_cmpk_gt_u32 s16, 0x8f
	s_mov_b32 m0, s88
	v_mfma_f32_16x16x32_f16 v[18:21], v[2:5], v[10:13], 0
	global_load_lds_dwordx4 v168, s[72:73]
	s_mov_b32 s5, s4
	s_cselect_b64 s[8:9], -1, 0
	s_cmpk_lt_u32 s16, 0x90
	v_mfma_f32_16x16x32_f16 v[26:29], v[2:5], v[14:17], 0
	s_mov_b32 m0, s89
	v_mfma_f32_16x16x32_f16 v[30:33], v[6:9], v[14:17], 0
	global_load_lds_dwordx4 v169, s[72:73]
	ds_read_b128 v[10:13], v136 offset:4096
	ds_read_b128 v[14:17], v136 offset:6144
	s_waitcnt lgkmcnt(0)
	v_mfma_f32_16x16x32_f16 v[34:37], v[2:5], v[10:13], 0
	s_mov_b32 m0, s90
	v_mfma_f32_16x16x32_f16 v[38:41], v[6:9], v[10:13], 0
	global_load_lds_dwordx4 v170, s[72:73]
	v_mfma_f32_16x16x32_f16 v[42:45], v[2:5], v[14:17], 0
	s_mov_b32 m0, s91
	v_mfma_f32_16x16x32_f16 v[46:49], v[6:9], v[14:17], 0
	global_load_lds_dwordx4 v171, s[72:73]
	ds_read_b128 v[10:13], v136 offset:8192
	ds_read_b128 v[14:17], v136 offset:10240
	s_waitcnt lgkmcnt(0)
	v_mfma_f32_16x16x32_f16 v[50:53], v[2:5], v[10:13], 0
	s_mov_b32 m0, s92
	v_mfma_f32_16x16x32_f16 v[54:57], v[6:9], v[10:13], 0
	global_load_lds_dwordx4 v172, s[74:75]
	ds_read_b128 v[10:13], v136 offset:12288
	ds_read_b128 v[82:85], v136 offset:14336
	v_mfma_f32_16x16x32_f16 v[58:61], v[2:5], v[14:17], 0
	s_mov_b32 m0, s93
	v_mfma_f32_16x16x32_f16 v[70:73], v[6:9], v[14:17], 0
	global_load_lds_dwordx4 v173, s[74:75]
	v_mov_b64_e32 v[16:17], s[6:7]
	v_mov_b64_e32 v[14:15], s[4:5]
	s_waitcnt lgkmcnt(0)
	v_mfma_f32_16x16x32_f16 v[66:69], v[2:5], v[10:13], 0
	v_mfma_f32_16x16x32_f16 v[74:77], v[6:9], v[10:13], 0
	v_mov_b64_e32 v[12:13], s[6:7]
	v_mov_b64_e32 v[10:11], s[4:5]
	v_mfma_f32_16x16x32_f16 v[78:81], v[2:5], v[82:85], 0
	v_mfma_f32_16x16x32_f16 v[82:85], v[6:9], v[82:85], 0
	s_cbranch_scc1 .LBB3_68
	ds_read_b128 v[14:17], v136 offset:16384
	s_waitcnt lgkmcnt(0)
	v_mfma_f32_16x16x32_f16 v[10:13], v[2:5], v[14:17], 0
	v_mfma_f32_16x16x32_f16 v[14:17], v[6:9], v[14:17], 0

.LBB3_81:
	v_add_u32_e32 v84, 0x5000, v109
	s_mov_b64 s[8:9], 0x180
	v_readfirstlane_b32 s12, v84
	v_add_u32_e32 v84, 0x7000, v109
	v_lshl_add_u64 v[82:83], v[100:101], 0, s[8:9]
	s_mov_b32 m0, s12
	v_readfirstlane_b32 s12, v84
	v_add_u32_e32 v84, 0x9000, v109
	s_barrier
	v_lshl_add_u64 v[82:83], v[98:99], 0, s[8:9]
	s_mov_b32 m0, s12
	v_readfirstlane_b32 s12, v84
	v_add_u32_e32 v84, 0xb000, v109
	v_lshl_add_u64 v[82:83], v[96:97], 0, s[8:9]
	s_mov_b32 m0, s12
	v_readfirstlane_b32 s12, v84
	v_lshl_add_u64 v[82:83], v[94:95], 0, s[8:9]
	s_mov_b32 m0, s12
	v_readfirstlane_b32 s12, v109
	v_add_u32_e32 v84, 0x2000, v109
	v_lshl_add_u64 v[82:83], v[104:105], 0, s[8:9]
	s_mov_b32 m0, s12
	v_readfirstlane_b32 s12, v84
	v_lshl_add_u64 v[82:83], v[102:103], 0, s[8:9]
	s_mov_b32 m0, s12
	s_and_b64 vcc, exec, s[2:3]
	s_cbranch_vccnz .LBB3_83
	v_add_u32_e32 v84, 0x4000, v109
	v_lshl_add_u64 v[82:83], v[106:107], 0, s[8:9]
	v_readfirstlane_b32 s8, v84
	s_mov_b32 m0, s8
	s_nop 0
	global_load_lds_dwordx4 v[82:83], off
.LBB3_83:
	s_add_u32 s72, s66, 0x180
	s_addc_u32 s73, s67, 0
	s_add_u32 s74, s68, 0x180
	s_addc_u32 s75, s69, 0
	v_add_u32_e32 v82, s18, v115
	v_add_u32_e32 v118, 0x5000, v82
	v_or_b32_e32 v115, v118, v116
	v_add_u32_e32 v124, 0, v115
	ds_read_b128 v[86:89], v124 offset:53248
	ds_read_b128 v[90:93], v124 offset:55296
	ds_read_b128 v[82:85], v136 offset:53248
	ds_read_b128 v[138:141], v136 offset:55296
	s_and_b64 vcc, exec, s[4:5]
	s_waitcnt lgkmcnt(0)
	v_mfma_f32_16x16x32_f16 v[18:21], v[86:89], v[82:85], v[18:21]
	s_mov_b32 m0, s76
	v_mfma_f32_16x16x32_f16 v[22:25], v[90:93], v[82:85], v[22:25]
	global_load_lds_dwordx4 v168, s[72:73]
	v_mfma_f32_16x16x32_f16 v[26:29], v[86:89], v[138:141], v[26:29]
	s_mov_b32 m0, s77
	v_mfma_f32_16x16x32_f16 v[30:33], v[90:93], v[138:141], v[30:33]
	global_load_lds_dwordx4 v169, s[72:73]
	ds_read_b128 v[82:85], v136 offset:57344
	ds_read_b128 v[138:141], v136 offset:59392
	s_waitcnt lgkmcnt(0)
	v_mfma_f32_16x16x32_f16 v[34:37], v[86:89], v[82:85], v[34:37]
	s_mov_b32 m0, s78
	v_mfma_f32_16x16x32_f16 v[38:41], v[90:93], v[82:85], v[38:41]
	global_load_lds_dwordx4 v170, s[72:73]
	v_mfma_f32_16x16x32_f16 v[42:45], v[86:89], v[138:141], v[42:45]
	s_mov_b32 m0, s79
	v_mfma_f32_16x16x32_f16 v[46:49], v[90:93], v[138:141], v[46:49]
	global_load_lds_dwordx4 v171, s[72:73]
	ds_read_b128 v[82:85], v136 offset:61440
	ds_read_b128 v[140:143], v136 offset:63488
	v_add_u32_e32 v138, 0xd000, v136
	s_waitcnt lgkmcnt(0)
	v_mfma_f32_16x16x32_f16 v[50:53], v[86:89], v[82:85], v[50:53]
	s_mov_b32 m0, s80
	v_mfma_f32_16x16x32_f16 v[54:57], v[90:93], v[82:85], v[54:57]
	global_load_lds_dwordx4 v172, s[74:75]
	v_mfma_f32_16x16x32_f16 v[62:65], v[86:89], v[140:143], v[62:65]
	s_mov_b32 m0, s81
	v_mfma_f32_16x16x32_f16 v[82:85], v[90:93], v[140:143], v[58:61]
	global_load_lds_dwordx4 v173, s[74:75]
	s_nop 2
	ds_read_b128 v[58:61], v138 offset:12288
	ds_read_b128 v[140:143], v138 offset:14336
	s_waitcnt lgkmcnt(0)
	v_mfma_f32_16x16x32_f16 v[66:69], v[86:89], v[58:61], v[66:69]
	v_mfma_f32_16x16x32_f16 v[70:73], v[90:93], v[58:61], v[70:73]
	v_mfma_f32_16x16x32_f16 v[74:77], v[86:89], v[140:143], v[74:77]
	v_mfma_f32_16x16x32_f16 v[78:81], v[90:93], v[140:143], v[78:81]
	s_cbranch_vccnz .LBB3_85
	ds_read_b128 v[58:61], v138 offset:16384
	s_waitcnt lgkmcnt(0)
	v_mfma_f32_16x16x32_f16 v[10:13], v[86:89], v[58:61], v[10:13]
	v_mfma_f32_16x16x32_f16 v[14:17], v[90:93], v[58:61], v[14:17]

.LBB3_92:
	s_mov_b64 s[8:9], 0x200
	v_readfirstlane_b32 s12, v110
	v_add_u32_e32 v166, 0x2000, v110
	v_lshl_add_u64 v[164:165], v[100:101], 0, s[8:9]
	s_mov_b32 m0, s12
	v_readfirstlane_b32 s12, v166
	v_add_u32_e32 v166, 0x4000, v110
	s_barrier
	s_waitcnt lgkmcnt(0)
	v_add_u32_e32 v90, s17, v115
	ds_read_b128 v[82:85], v90
	ds_read_b128 v[86:89], v90 offset:2048
	v_add_u32_e32 v125, s17, v113
	ds_read_b128 v[118:121], v125
	ds_read_b128 v[142:145], v125 offset:2048
	ds_read_b128 v[148:151], v125 offset:4096
	ds_read_b128 v[152:155], v125 offset:6144
	ds_read_b128 v[156:159], v125 offset:8192
	ds_read_b128 v[160:163], v125 offset:10240
	v_lshl_add_u64 v[164:165], v[98:99], 0, s[8:9]
	s_mov_b32 m0, s12
	v_readfirstlane_b32 s12, v166
	v_add_u32_e32 v166, 0x6000, v110
	v_lshl_add_u64 v[164:165], v[96:97], 0, s[8:9]
	s_mov_b32 m0, s12
	v_readfirstlane_b32 s12, v166
	v_add_u32_e32 v166, 0xd000, v109
	v_lshl_add_u64 v[164:165], v[94:95], 0, s[8:9]
	s_mov_b32 m0, s12
	v_readfirstlane_b32 s12, v166
	v_add_u32_e32 v166, 0xf000, v109
	v_lshl_add_u64 v[164:165], v[104:105], 0, s[8:9]
	s_mov_b32 m0, s12
	v_readfirstlane_b32 s12, v166
	v_lshl_add_u64 v[164:165], v[102:103], 0, s[8:9]
	s_mov_b32 m0, s12
	s_and_b64 vcc, exec, s[2:3]
	s_cbranch_vccnz .LBB3_94
	v_lshl_add_u64 v[164:165], v[106:107], 0, s[8:9]
	s_add_i32 s8, 0, 0x11000
	v_add_u32_e32 v166, s8, v108
	s_nop 0
	v_readfirstlane_b32 s8, v166
	s_mov_b32 m0, s8
	s_nop 0
	global_load_lds_dwordx4 v[164:165], off
.LBB3_94:
	s_add_u32 s72, s66, 0x200
	s_addc_u32 s73, s67, 0
	s_add_u32 s74, s68, 0x200
	s_addc_u32 s75, s69, 0
	s_and_b64 vcc, exec, s[4:5]
	s_waitcnt lgkmcnt(5)
	v_mfma_f32_16x16x32_f16 v[22:25], v[86:89], v[118:121], v[22:25]
	s_mov_b32 m0, s82
	v_mfma_f32_16x16x32_f16 v[18:21], v[82:85], v[118:121], v[18:21]
	global_load_lds_dwordx4 v168, s[72:73]
	s_waitcnt lgkmcnt(4)
	v_mfma_f32_16x16x32_f16 v[26:29], v[82:85], v[142:145], v[26:29]
	s_mov_b32 m0, s83
	v_mfma_f32_16x16x32_f16 v[30:33], v[86:89], v[142:145], v[30:33]
	global_load_lds_dwordx4 v169, s[72:73]
	s_waitcnt lgkmcnt(3)
	v_mfma_f32_16x16x32_f16 v[34:37], v[82:85], v[148:151], v[34:37]
	s_mov_b32 m0, s84
	v_mfma_f32_16x16x32_f16 v[38:41], v[86:89], v[148:151], v[38:41]
	global_load_lds_dwordx4 v170, s[72:73]
	ds_read_b128 v[148:151], v125 offset:12288
	s_waitcnt lgkmcnt(3)
	v_mfma_f32_16x16x32_f16 v[42:45], v[82:85], v[152:155], v[42:45]
	s_mov_b32 m0, s85
	v_mfma_f32_16x16x32_f16 v[46:49], v[86:89], v[152:155], v[46:49]
	global_load_lds_dwordx4 v171, s[72:73]
	ds_read_b128 v[152:155], v125 offset:14336
	s_waitcnt lgkmcnt(3)
	v_mfma_f32_16x16x32_f16 v[50:53], v[82:85], v[156:159], v[50:53]
	s_mov_b32 m0, s86
	v_mfma_f32_16x16x32_f16 v[54:57], v[86:89], v[156:159], v[54:57]
	global_load_lds_dwordx4 v172, s[74:75]
	s_waitcnt lgkmcnt(2)
	v_mfma_f32_16x16x32_f16 v[58:61], v[82:85], v[160:163], v[58:61]
	s_mov_b32 m0, s87
	v_mfma_f32_16x16x32_f16 v[62:65], v[86:89], v[160:163], v[62:65]
	global_load_lds_dwordx4 v173, s[74:75]
	s_waitcnt lgkmcnt(1)
	v_mfma_f32_16x16x32_f16 v[66:69], v[82:85], v[148:151], v[66:69]
	v_mfma_f32_16x16x32_f16 v[70:73], v[86:89], v[148:151], v[70:73]
	s_waitcnt lgkmcnt(0)
	v_mfma_f32_16x16x32_f16 v[74:77], v[82:85], v[152:155], v[74:77]
	v_mfma_f32_16x16x32_f16 v[78:81], v[86:89], v[152:155], v[78:81]
	s_cbranch_vccnz .LBB3_96
	ds_read_b128 v[118:121], v125 offset:16384
	s_waitcnt lgkmcnt(0)
	v_mfma_f32_16x16x32_f16 v[10:13], v[82:85], v[118:121], v[10:13]
	v_mfma_f32_16x16x32_f16 v[14:17], v[86:89], v[118:121], v[14:17]

.LBB3_106:
	s_mov_b64 s[10:11], 0x280
	v_readfirstlane_b32 s12, v111
	v_add_u32_e32 v84, 0x2000, v111
	v_lshl_add_u64 v[82:83], v[100:101], 0, s[10:11]
	s_mov_b32 m0, s12
	v_readfirstlane_b32 s12, v84
	v_add_u32_e32 v84, 0x4000, v111
	s_barrier
	v_lshl_add_u64 v[82:83], v[98:99], 0, s[10:11]
	s_mov_b32 m0, s12
	v_readfirstlane_b32 s12, v84
	v_add_u32_e32 v84, 0x6000, v111
	v_lshl_add_u64 v[82:83], v[96:97], 0, s[10:11]
	s_mov_b32 m0, s12
	v_readfirstlane_b32 s12, v84
	v_lshl_add_u64 v[82:83], v[94:95], 0, s[10:11]
	s_mov_b32 m0, s12
	v_readfirstlane_b32 s12, v112
	v_add_u32_e32 v84, 0x2000, v112
	v_lshl_add_u64 v[82:83], v[104:105], 0, s[10:11]
	s_mov_b32 m0, s12
	v_readfirstlane_b32 s12, v84
	v_lshl_add_u64 v[82:83], v[102:103], 0, s[10:11]
	s_mov_b32 m0, s12
	s_and_b64 vcc, exec, s[2:3]
	s_cbranch_vccnz .LBB3_108
	v_lshl_add_u64 v[82:83], v[106:107], 0, s[10:11]
	s_add_i32 s10, 0, 0x1e000
	v_add_u32_e32 v84, s10, v108
	s_nop 0
	v_readfirstlane_b32 s10, v84
	s_mov_b32 m0, s10
	s_nop 0
	global_load_lds_dwordx4 v[82:83], off
.LBB3_108:
	s_add_u32 s72, s66, 0x280
	s_addc_u32 s73, s67, 0
	s_add_u32 s74, s68, 0x280
	s_addc_u32 s75, s69, 0
	s_waitcnt lgkmcnt(0)
	ds_read_b128 v[82:85], v122 offset:20480
	ds_read_b128 v[86:89], v122 offset:22528
	ds_read_b128 v[112:115], v136
	ds_read_b128 v[116:119], v136 offset:2048
	ds_read_b128 v[148:151], v136 offset:4096
	ds_read_b128 v[152:155], v136 offset:6144
	ds_read_b128 v[156:159], v136 offset:8192
	ds_read_b128 v[160:163], v136 offset:10240
	s_and_b64 vcc, exec, s[4:5]
	s_waitcnt lgkmcnt(5)
	v_mfma_f32_16x16x32_f16 v[18:21], v[82:85], v[112:115], v[18:21]
	s_mov_b32 m0, s88
	v_mfma_f32_16x16x32_f16 v[22:25], v[86:89], v[112:115], v[22:25]
	global_load_lds_dwordx4 v168, s[72:73]
	s_waitcnt lgkmcnt(4)
	v_mfma_f32_16x16x32_f16 v[26:29], v[82:85], v[116:119], v[26:29]
	s_mov_b32 m0, s89
	v_mfma_f32_16x16x32_f16 v[30:33], v[86:89], v[116:119], v[30:33]
	global_load_lds_dwordx4 v169, s[72:73]
	s_waitcnt lgkmcnt(3)
	v_mfma_f32_16x16x32_f16 v[34:37], v[82:85], v[148:151], v[34:37]
	s_mov_b32 m0, s90
	v_mfma_f32_16x16x32_f16 v[38:41], v[86:89], v[148:151], v[38:41]
	global_load_lds_dwordx4 v170, s[72:73]
	ds_read_b128 v[148:151], v136 offset:12288
	s_waitcnt lgkmcnt(3)
	v_mfma_f32_16x16x32_f16 v[42:45], v[82:85], v[152:155], v[42:45]
	s_mov_b32 m0, s91
	v_mfma_f32_16x16x32_f16 v[46:49], v[86:89], v[152:155], v[46:49]
	global_load_lds_dwordx4 v171, s[72:73]
	ds_read_b128 v[152:155], v136 offset:14336
	s_waitcnt lgkmcnt(3)
	v_mfma_f32_16x16x32_f16 v[50:53], v[82:85], v[156:159], v[50:53]
	s_mov_b32 m0, s92
	v_mfma_f32_16x16x32_f16 v[54:57], v[86:89], v[156:159], v[54:57]
	global_load_lds_dwordx4 v172, s[74:75]
	s_waitcnt lgkmcnt(2)
	v_mfma_f32_16x16x32_f16 v[58:61], v[82:85], v[160:163], v[58:61]
	s_mov_b32 m0, s93
	v_mfma_f32_16x16x32_f16 v[62:65], v[86:89], v[160:163], v[62:65]
	global_load_lds_dwordx4 v173, s[74:75]
	s_waitcnt lgkmcnt(1)
	v_mfma_f32_16x16x32_f16 v[66:69], v[82:85], v[148:151], v[66:69]
	v_mfma_f32_16x16x32_f16 v[70:73], v[86:89], v[148:151], v[70:73]
	s_waitcnt lgkmcnt(0)
	v_mfma_f32_16x16x32_f16 v[74:77], v[82:85], v[152:155], v[74:77]
	v_mfma_f32_16x16x32_f16 v[78:81], v[86:89], v[152:155], v[78:81]
	s_cbranch_vccnz .LBB3_110
	ds_read_b128 v[112:115], v136 offset:16384
	s_waitcnt lgkmcnt(0)
	v_mfma_f32_16x16x32_f16 v[10:13], v[82:85], v[112:115], v[10:13]
	v_mfma_f32_16x16x32_f16 v[14:17], v[86:89], v[112:115], v[14:17]

.LBB3_117:
	v_add_u32_e32 v166, 0x5000, v109
	s_mov_b64 s[10:11], 0x300
	v_readfirstlane_b32 s12, v166
	v_add_u32_e32 v166, 0x7000, v109
	v_lshl_add_u64 v[164:165], v[100:101], 0, s[10:11]
	s_mov_b32 m0, s12
	v_readfirstlane_b32 s12, v166
	v_add_u32_e32 v166, 0x9000, v109
	s_barrier
	s_waitcnt lgkmcnt(0)
	ds_read_b128 v[82:85], v124 offset:53248
	ds_read_b128 v[86:89], v124 offset:55296
	ds_read_b128 v[112:115], v136 offset:53248
	ds_read_b128 v[116:119], v136 offset:55296
	ds_read_b128 v[148:151], v136 offset:57344
	ds_read_b128 v[152:155], v136 offset:59392
	ds_read_b128 v[156:159], v136 offset:61440
	ds_read_b128 v[160:163], v136 offset:63488
	v_lshl_add_u64 v[164:165], v[98:99], 0, s[10:11]
	s_mov_b32 m0, s12
	v_readfirstlane_b32 s12, v166
	v_add_u32_e32 v166, 0xb000, v109
	v_lshl_add_u64 v[164:165], v[96:97], 0, s[10:11]
	s_mov_b32 m0, s12
	v_readfirstlane_b32 s12, v166
	v_lshl_add_u64 v[164:165], v[94:95], 0, s[10:11]
	s_mov_b32 m0, s12
	v_readfirstlane_b32 s12, v109
	v_add_u32_e32 v166, 0x2000, v109
	v_lshl_add_u64 v[164:165], v[104:105], 0, s[10:11]
	s_mov_b32 m0, s12
	v_readfirstlane_b32 s12, v166
	v_lshl_add_u64 v[164:165], v[102:103], 0, s[10:11]
	s_mov_b32 m0, s12
	s_and_b64 vcc, exec, s[2:3]
	s_cbranch_vccnz .LBB3_119
	v_add_u32_e32 v166, 0x4000, v109
	v_lshl_add_u64 v[164:165], v[106:107], 0, s[10:11]
	v_readfirstlane_b32 s10, v166
	s_mov_b32 m0, s10
	s_nop 0
	global_load_lds_dwordx4 v[164:165], off
.LBB3_119:
	s_add_u32 s72, s66, 0x300
	s_addc_u32 s73, s67, 0
	s_add_u32 s74, s68, 0x300
	s_addc_u32 s75, s69, 0
	s_and_b64 vcc, exec, s[4:5]
	s_waitcnt lgkmcnt(5)
	v_mfma_f32_16x16x32_f16 v[18:21], v[82:85], v[112:115], v[18:21]
	s_mov_b32 m0, s76
	v_mfma_f32_16x16x32_f16 v[22:25], v[86:89], v[112:115], v[22:25]
	global_load_lds_dwordx4 v168, s[72:73]
	s_waitcnt lgkmcnt(4)
	v_mfma_f32_16x16x32_f16 v[26:29], v[82:85], v[116:119], v[26:29]
	s_mov_b32 m0, s77
	v_mfma_f32_16x16x32_f16 v[30:33], v[86:89], v[116:119], v[30:33]
	global_load_lds_dwordx4 v169, s[72:73]
	s_waitcnt lgkmcnt(3)
	v_mfma_f32_16x16x32_f16 v[34:37], v[82:85], v[148:151], v[34:37]
	s_mov_b32 m0, s78
	v_mfma_f32_16x16x32_f16 v[38:41], v[86:89], v[148:151], v[38:41]
	global_load_lds_dwordx4 v170, s[72:73]
	ds_read_b128 v[148:151], v138 offset:12288
	s_waitcnt lgkmcnt(3)
	v_mfma_f32_16x16x32_f16 v[42:45], v[82:85], v[152:155], v[42:45]
	s_mov_b32 m0, s79
	v_mfma_f32_16x16x32_f16 v[46:49], v[86:89], v[152:155], v[46:49]
	global_load_lds_dwordx4 v171, s[72:73]
	ds_read_b128 v[152:155], v138 offset:14336
	s_waitcnt lgkmcnt(3)
	v_mfma_f32_16x16x32_f16 v[50:53], v[82:85], v[156:159], v[50:53]
	s_mov_b32 m0, s80
	v_mfma_f32_16x16x32_f16 v[54:57], v[86:89], v[156:159], v[54:57]
	global_load_lds_dwordx4 v172, s[74:75]
	s_waitcnt lgkmcnt(2)
	v_mfma_f32_16x16x32_f16 v[58:61], v[82:85], v[160:163], v[58:61]
	s_mov_b32 m0, s81
	v_mfma_f32_16x16x32_f16 v[62:65], v[86:89], v[160:163], v[62:65]
	global_load_lds_dwordx4 v173, s[74:75]
	s_waitcnt lgkmcnt(1)
	v_mfma_f32_16x16x32_f16 v[66:69], v[82:85], v[148:151], v[66:69]
	v_mfma_f32_16x16x32_f16 v[70:73], v[86:89], v[148:151], v[70:73]
	s_waitcnt lgkmcnt(0)
	v_mfma_f32_16x16x32_f16 v[74:77], v[82:85], v[152:155], v[74:77]
	v_mfma_f32_16x16x32_f16 v[78:81], v[86:89], v[152:155], v[78:81]
	s_cbranch_vccnz .LBB3_121
	ds_read_b128 v[112:115], v138 offset:16384
	s_waitcnt lgkmcnt(0)
	v_mfma_f32_16x16x32_f16 v[10:13], v[82:85], v[112:115], v[10:13]
	v_mfma_f32_16x16x32_f16 v[14:17], v[86:89], v[112:115], v[14:17]

.LBB3_128:
	s_mov_b64 s[10:11], 0x380
	v_readfirstlane_b32 s12, v110
	v_add_u32_e32 v166, 0x2000, v110
	v_lshl_add_u64 v[164:165], v[100:101], 0, s[10:11]
	s_mov_b32 m0, s12
	v_readfirstlane_b32 s12, v166
	v_add_u32_e32 v166, 0x4000, v110
	s_barrier
	s_waitcnt lgkmcnt(0)
	ds_read_b128 v[114:117], v90
	ds_read_b128 v[118:121], v90 offset:2048
	ds_read_b128 v[82:85], v125
	ds_read_b128 v[86:89], v125 offset:2048
	ds_read_b128 v[148:151], v125 offset:4096
	ds_read_b128 v[152:155], v125 offset:6144
	ds_read_b128 v[156:159], v125 offset:8192
	ds_read_b128 v[160:163], v125 offset:10240
	v_lshl_add_u64 v[164:165], v[98:99], 0, s[10:11]
	s_mov_b32 m0, s12
	v_readfirstlane_b32 s12, v166
	v_add_u32_e32 v166, 0x6000, v110
	v_lshl_add_u64 v[164:165], v[96:97], 0, s[10:11]
	s_mov_b32 m0, s12
	v_readfirstlane_b32 s12, v166
	v_add_u32_e32 v166, 0xd000, v109
	v_lshl_add_u64 v[164:165], v[94:95], 0, s[10:11]
	s_mov_b32 m0, s12
	v_readfirstlane_b32 s12, v166
	v_add_u32_e32 v166, 0xf000, v109
	v_lshl_add_u64 v[164:165], v[104:105], 0, s[10:11]
	s_mov_b32 m0, s12
	v_readfirstlane_b32 s12, v166
	v_lshl_add_u64 v[164:165], v[102:103], 0, s[10:11]
	s_mov_b32 m0, s12
	s_and_b64 vcc, exec, s[2:3]
	s_cbranch_vccnz .LBB3_130
	s_add_i32 s2, 0, 0x11000
	v_add_u32_e32 v166, s2, v108
	v_lshl_add_u64 v[164:165], v[106:107], 0, s[10:11]
	v_readfirstlane_b32 s2, v166
	s_mov_b32 m0, s2
	s_nop 0
	global_load_lds_dwordx4 v[164:165], off
.LBB3_130:
	s_add_u32 s72, s66, 0x380
	s_addc_u32 s73, s67, 0
	s_add_u32 s74, s68, 0x380
	s_addc_u32 s75, s69, 0
	s_and_b64 vcc, exec, s[4:5]
	s_waitcnt lgkmcnt(5)
	v_mfma_f32_16x16x32_f16 v[18:21], v[114:117], v[82:85], v[18:21]
	s_mov_b32 m0, s82
	v_mfma_f32_16x16x32_f16 v[22:25], v[118:121], v[82:85], v[22:25]
	global_load_lds_dwordx4 v168, s[72:73]
	s_waitcnt lgkmcnt(4)
	v_mfma_f32_16x16x32_f16 v[26:29], v[114:117], v[86:89], v[26:29]
	s_mov_b32 m0, s83
	v_mfma_f32_16x16x32_f16 v[30:33], v[118:121], v[86:89], v[30:33]
	global_load_lds_dwordx4 v169, s[72:73]
	s_waitcnt lgkmcnt(2)
	v_mfma_f32_16x16x32_f16 v[42:45], v[114:117], v[152:155], v[42:45]
	s_mov_b32 m0, s84
	v_mfma_f32_16x16x32_f16 v[46:49], v[118:121], v[152:155], v[46:49]
	global_load_lds_dwordx4 v170, s[72:73]
	v_mfma_f32_16x16x32_f16 v[34:37], v[114:117], v[148:151], v[34:37]
	s_mov_b32 m0, s85
	v_mfma_f32_16x16x32_f16 v[38:41], v[118:121], v[148:151], v[38:41]
	global_load_lds_dwordx4 v171, s[72:73]
	ds_read_b128 v[148:151], v125 offset:12288
	ds_read_b128 v[152:155], v125 offset:14336
	s_waitcnt lgkmcnt(3)
	v_mfma_f32_16x16x32_f16 v[82:85], v[114:117], v[156:159], v[50:53]
	s_mov_b32 m0, s86
	v_mfma_f32_16x16x32_f16 v[86:89], v[118:121], v[156:159], v[54:57]
	global_load_lds_dwordx4 v172, s[74:75]
	s_nop 1
	s_waitcnt lgkmcnt(2)
	v_mfma_f32_16x16x32_f16 v[90:93], v[114:117], v[160:163], v[58:61]
	s_mov_b32 m0, s87
	v_mfma_f32_16x16x32_f16 v[94:97], v[118:121], v[160:163], v[62:65]
	global_load_lds_dwordx4 v173, s[74:75]
	s_waitcnt lgkmcnt(1)
	v_mfma_f32_16x16x32_f16 v[98:101], v[114:117], v[148:151], v[66:69]
	v_mfma_f32_16x16x32_f16 v[102:105], v[118:121], v[148:151], v[70:73]
	s_waitcnt lgkmcnt(0)
	v_mfma_f32_16x16x32_f16 v[106:109], v[114:117], v[152:155], v[74:77]
	v_mfma_f32_16x16x32_f16 v[110:113], v[118:121], v[152:155], v[78:81]
	s_cbranch_vccnz .LBB3_132
	ds_read_b128 v[50:53], v125 offset:16384
	s_waitcnt lgkmcnt(0)
	v_mfma_f32_16x16x32_f16 v[10:13], v[114:117], v[50:53], v[10:13]
	v_mfma_f32_16x16x32_f16 v[14:17], v[118:121], v[50:53], v[14:17]

	.amdhsa_kernel _Z8moe_gemmILi1EEvPKDF16_S1_PvPKyPKiPKfS1_
		.amdhsa_group_segment_fixed_size 0
		.amdhsa_private_segment_fixed_size 0
		.amdhsa_kernarg_size 56
		.amdhsa_user_sgpr_count 2
		.amdhsa_user_sgpr_dispatch_ptr 0
		.amdhsa_user_sgpr_queue_ptr 0
		.amdhsa_user_sgpr_kernarg_segment_ptr 1
		.amdhsa_user_sgpr_dispatch_id 0
		.amdhsa_user_sgpr_kernarg_preload_length 0
		.amdhsa_user_sgpr_kernarg_preload_offset 0
		.amdhsa_user_sgpr_private_segment_size 0
		.amdhsa_uses_dynamic_stack 0
		.amdhsa_enable_private_segment 0
		.amdhsa_system_sgpr_workgroup_id_x 1
		.amdhsa_system_sgpr_workgroup_id_y 0
		.amdhsa_system_sgpr_workgroup_id_z 0
		.amdhsa_system_sgpr_workgroup_info 0
		.amdhsa_system_vgpr_workitem_id 0
		.amdhsa_next_free_vgpr 176
		.amdhsa_next_free_sgpr 94
		.amdhsa_accum_offset 176
		.amdhsa_reserve_vcc 1
		.amdhsa_float_round_mode_32 0
		.amdhsa_float_round_mode_16_64 0
		.amdhsa_float_denorm_mode_32 3
		.amdhsa_float_denorm_mode_16_64 3
		.amdhsa_dx10_clamp 1
		.amdhsa_ieee_mode 1
		.amdhsa_fp16_overflow 0
		.amdhsa_tg_split 0
		.amdhsa_exception_fp_ieee_invalid_op 0
		.amdhsa_exception_fp_denorm_src 0
		.amdhsa_exception_fp_ieee_div_zero 0
		.amdhsa_exception_fp_ieee_overflow 0
		.amdhsa_exception_fp_ieee_underflow 0
		.amdhsa_exception_fp_ieee_inexact 0
		.amdhsa_exception_int_div_zero 0
	.end_amdhsa_kernel

.LBB4_35:
	s_abs_i32 s3, s26
	v_cvt_f32_u32_e32 v1, s3
	s_sub_i32 s11, 0, s3
	s_lshl_b32 s10, s19, 2
	s_add_i32 s17, s12, -1
	v_rcp_iflag_f32_e32 v1, v1
	s_sub_i32 s24, s18, s10
	s_add_i32 s10, s17, s26
	s_xor_b32 s14, s10, s26
	v_mul_f32_e32 v1, 0x4f7ffffe, v1
	v_cvt_u32_f32_e32 v1, v1
	s_abs_i32 s10, s10
	s_ashr_i32 s14, s14, 31
	v_lshrrev_b32_e32 v7, 3, v0
	v_readfirstlane_b32 s15, v1
	s_mul_i32 s11, s11, s15
	s_mul_hi_u32 s11, s15, s11
	s_add_i32 s15, s15, s11
	s_mul_hi_u32 s11, s10, s15
	s_mul_i32 s15, s11, s3
	s_sub_i32 s10, s10, s15
	s_add_i32 s16, s11, 1
	s_sub_i32 s15, s10, s3
	s_cmp_ge_u32 s10, s3
	s_cselect_b32 s11, s16, s11
	s_cselect_b32 s10, s15, s10
	s_add_i32 s15, s11, 1
	s_cmp_ge_u32 s10, s3
	s_cselect_b32 s3, s15, s11
	s_xor_b32 s3, s3, s14
	s_sub_i32 s34, s3, s14
	s_add_i32 s34, s34, 15
	s_and_b32 s10, s34, -16
	s_mul_i32 s11, s10, s2
	v_add_u32_e32 v9, s11, v7
	s_lshl_b32 s16, s13, 13
	v_min_i32_e32 v1, s17, v9
	v_add_u32_e32 v2, s16, v1
	v_add_u32_e32 v1, 64, v9
	v_min_i32_e32 v1, s17, v1
	v_ashrrev_i32_e32 v3, 31, v2
	v_add_u32_e32 v4, s16, v1
	s_waitcnt lgkmcnt(0)
	v_lshl_add_u64 v[2:3], v[2:3], 2, s[8:9]
	v_ashrrev_i32_e32 v5, 31, v4
	v_lshl_add_u64 v[4:5], v[4:5], 2, s[8:9]
	global_load_dword v6, v[2:3], off
	global_load_dword v8, v[4:5], off
	v_add_u32_e32 v152, 0x80, v9
	v_min_i32_e32 v152, s17, v152
	v_add_u32_e32 v152, s16, v152
	v_ashrrev_i32_e32 v153, 31, v152
	v_lshl_add_u64 v[152:153], v[152:153], 2, s[8:9]
	global_load_dword v152, v[152:153], off
	v_lshlrev_b32_e32 v1, 4, v0
	v_add_u32_e32 v135, 0, v1
	s_lshl_b32 s14, s13, 10
	s_lshl_b32 s13, s24, 8
	v_add_u32_e32 v4, 0x5000, v135
	v_add_u32_e32 v5, 0x7000, v135
	s_ashr_i32 s29, s13, 31
	s_mov_b32 s15, 0
	v_readfirstlane_b32 s25, v4
	v_readfirstlane_b32 s26, v5
	v_or_b32_e32 v4, s13, v7
	v_mov_b32_e32 v5, s29
	v_xor_b32_e32 v2, v7, v0
	s_add_i32 s24, 0, 0x12000
	v_lshl_add_u64 v[4:5], v[4:5], 0, s[14:15]
	v_lshlrev_b32_e32 v2, 4, v2
	v_add_u32_e32 v10, 0x9000, v135
	v_add_u32_e32 v11, 0xb000, v135
	v_add_u32_e32 v136, s24, v1
	v_lshlrev_b64 v[4:5], 10, v[4:5]
	v_mov_b32_e32 v3, 0
	v_and_b32_e32 v2, 0x70, v2
	v_readfirstlane_b32 s27, v10
	v_readfirstlane_b32 s28, v11
	v_add_u32_e32 v7, 0x2000, v136
	s_mov_b64 s[66:67], s[6:7]
	v_lshl_add_u64 v[10:11], s[6:7], 0, v[4:5]
	s_mov_b64 s[18:19], 0x10000
	v_readfirstlane_b32 s14, v7
	v_or_b32_e32 v4, 0x20000, v4
	v_lshl_add_u64 v[116:117], v[10:11], 0, v[2:3]
	v_add_u32_e32 v7, 0x80, v9
	s_mov_b32 m0, s25
	v_lshl_add_u64 v[4:5], s[6:7], 0, v[4:5]
	v_lshl_add_u64 v[114:115], v[116:117], 0, s[18:19]
	global_load_lds_dwordx4 v[116:117], off
	v_min_i32_e32 v7, s17, v7
	s_mov_b32 m0, s26
	s_mov_b64 s[20:21], 0x30000
	v_lshl_add_u64 v[112:113], v[4:5], 0, v[2:3]
	global_load_lds_dwordx4 v[114:115], off
	v_add_u32_e32 v14, s16, v7
	s_mov_b32 m0, s27
	s_mov_b64 s[2:3], 0x80
	v_readfirstlane_b32 s24, v136
	v_lshl_add_u64 v[110:111], v[116:117], 0, s[20:21]
	global_load_lds_dwordx4 v[112:113], off
	v_ashrrev_i32_e32 v15, 31, v14
	s_mov_b32 m0, s28
	s_mov_b64 s[22:23], 0x10080
	v_add_u32_e32 v16, 0x4000, v136
	v_lshl_add_u64 v[4:5], v[116:117], 0, s[2:3]
	global_load_lds_dwordx4 v[110:111], off
	v_lshl_add_u64 v[14:15], v[14:15], 2, s[8:9]
	s_mov_b32 m0, s24
	v_lshl_add_u64 v[10:11], v[116:117], 0, s[22:23]
	global_load_lds_dwordx4 v[4:5], off
	s_mov_b32 m0, s14
	v_readfirstlane_b32 s6, v16
	global_load_lds_dwordx4 v[10:11], off
	s_mov_b32 m0, s6
	s_mov_b64 s[6:7], 0x30080
	v_add_u32_e32 v5, 0x6000, v136
	v_lshl_add_u64 v[12:13], v[112:113], 0, s[2:3]
	v_lshl_add_u64 v[10:11], v[116:117], 0, s[6:7]
	v_readfirstlane_b32 s6, v5
	global_load_lds_dwordx4 v[12:13], off
	s_mov_b32 m0, s6
	v_readfirstlane_b32 s6, v135
	v_add_u32_e32 v5, 0x2000, v135
	global_load_lds_dwordx4 v[10:11], off
	s_waitcnt vmcnt(8)
	s_mov_b64 s[68:69], s[4:5]
	v_mov_b32_e32 v4, v152
	v_ashrrev_i32_e32 v7, 31, v6
	v_lshlrev_b64 v[6:7], 10, v[6:7]
	v_ashrrev_i32_e32 v9, 31, v8
	v_lshl_add_u64 v[6:7], s[4:5], 0, v[6:7]
	v_lshl_add_u64 v[120:121], v[6:7], 0, v[2:3]
	v_lshlrev_b64 v[6:7], 10, v[8:9]
	v_lshl_add_u64 v[6:7], s[4:5], 0, v[6:7]
	s_mov_b32 m0, s6
	v_readfirstlane_b32 s6, v5
	v_lshl_add_u64 v[118:119], v[6:7], 0, v[2:3]
	global_load_lds_dwordx4 v[120:121], off
	s_mov_b32 m0, s6
	s_lshr_b32 s6, s34, 3
	global_load_lds_dwordx4 v[118:119], off
	v_readfirstlane_b32 s27, v0
	s_and_b32 s6, s6, 0x1ffffffe
	s_lshr_b32 s26, s27, 6
	s_add_i32 s6, s6, -16
	s_cmp_lt_i32 s26, s6
	v_ashrrev_i32_e32 v5, 31, v4
	v_lshlrev_b64 v[4:5], 10, v[4:5]
	v_lshl_add_u64 v[4:5], s[4:5], 0, v[4:5]
	s_cselect_b64 s[4:5], -1, 0
	s_cmp_ge_i32 s26, s6
	s_cselect_b64 s[30:31], -1, 0
	v_lshl_add_u64 v[122:123], v[4:5], 0, v[2:3]
	s_and_b64 vcc, exec, s[30:31]
	s_cbranch_vccnz .LBB4_37
	v_add_u32_e32 v2, 0x4000, v135
	s_nop 0
	v_readfirstlane_b32 s6, v2
	s_mov_b32 m0, s6
	s_nop 0
	global_load_lds_dwordx4 v[122:123], off

.LBB4_85:
	s_add_i32 s27, 0, 0x1f000
	v_add_u32_e32 v144, s27, v1
	s_mov_b64 s[24:25], 0x100
	v_readfirstlane_b32 s27, v144
	v_add_u32_e32 v23, 0x2000, v144
	v_lshl_add_u64 v[34:35], v[116:117], 0, s[24:25]
	s_mov_b32 m0, s27
	v_readfirstlane_b32 s27, v23
	v_add_u32_e32 v23, 0x4000, v144
	v_readfirstlane_b32 s70, v0
	s_nop 3
	s_lshr_b32 s70, s70, 6
	s_lshl_b32 s70, s70, 10
	s_add_i32 s76, s70, 0x5000
	s_add_i32 s77, s70, 0x7000
	s_add_i32 s78, s70, 0x9000
	s_add_i32 s79, s70, 0xb000
	s_add_i32 s80, s70, 0x0
	s_add_i32 s81, s70, 0x2000
	s_add_i32 s82, s70, 0x12000
	s_add_i32 s83, s70, 0x14000
	s_add_i32 s84, s70, 0x16000
	s_add_i32 s85, s70, 0x18000
	s_add_i32 s86, s70, 0xd000
	s_add_i32 s87, s70, 0xf000
	s_add_i32 s88, s70, 0x1f000
	s_add_i32 s89, s70, 0x21000
	s_add_i32 s90, s70, 0x23000
	s_add_i32 s91, s70, 0x25000
	s_add_i32 s92, s70, 0x1a000
	s_add_i32 s93, s70, 0x1c000
	v_subrev_u32_e32 v176, s66, v116
	v_subrev_u32_e32 v177, s66, v114
	v_subrev_u32_e32 v178, s66, v112
	v_subrev_u32_e32 v179, s66, v110
	v_subrev_u32_e32 v180, s68, v120
	v_subrev_u32_e32 v181, s68, v118
	s_barrier
	v_lshl_add_u64 v[34:35], v[114:115], 0, s[24:25]
	s_mov_b32 m0, s27
	v_readfirstlane_b32 s27, v23
	v_add_u32_e32 v23, 0x6000, v144
	s_add_i32 s35, 0, 0x1a000
	v_lshl_add_u64 v[34:35], v[112:113], 0, s[24:25]
	s_mov_b32 m0, s27
	v_readfirstlane_b32 s27, v23
	v_add_u32_e32 v145, s35, v1
	v_lshl_add_u64 v[34:35], v[110:111], 0, s[24:25]
	s_mov_b32 m0, s27
	v_readfirstlane_b32 s27, v145
	v_add_u32_e32 v23, 0x2000, v145
	v_lshl_add_u64 v[34:35], v[120:121], 0, s[24:25]
	s_mov_b32 m0, s27
	v_readfirstlane_b32 s27, v23
	v_lshl_add_u64 v[34:35], v[118:119], 0, s[24:25]
	s_mov_b32 m0, s27
	s_and_b64 vcc, exec, s[14:15]
	s_cbranch_vccnz .LBB4_87
	v_lshl_add_u64 v[34:35], v[122:123], 0, s[24:25]
	s_add_i32 s24, 0, 0x1e000
	v_add_u32_e32 v23, s24, v1
	s_nop 0
	v_readfirstlane_b32 s24, v23
	s_mov_b32 m0, s24
	s_nop 0
	global_load_lds_dwordx4 v[34:35], off
.LBB4_87:
	s_add_u32 s72, s66, 0x100
	s_addc_u32 s73, s67, 0
	s_add_u32 s74, s68, 0x100
	s_addc_u32 s75, s69, 0
	v_lshlrev_b32_e32 v140, 7, v42
	s_lshl_b32 s36, s26, 12
	v_bitop3_b32 v23, v102, v0, 7 bitop3:0x78
	v_lshlrev_b32_e32 v141, 4, v23
	v_or_b32_e32 v34, s36, v140
	v_or_b32_e32 v23, v34, v141
	v_add_u32_e32 v138, 0, v23
	ds_read_b128 v[50:53], v138 offset:20480
	v_or_b32_e32 v146, v141, v140
	v_add_u32_e32 v137, 0, v146
	ds_read_b128 v[58:61], v137
	ds_read_b128 v[62:65], v138 offset:22528
	v_cvt_f32_f16_sdwa v45, v43 dst_sel:DWORD dst_unused:UNUSED_PAD src0_sel:WORD_1
	v_cvt_f32_f16_e32 v44, v43
	v_cvt_f32_f16_sdwa v47, v6 dst_sel:DWORD dst_unused:UNUSED_PAD src0_sel:WORD_1
	v_cvt_f32_f16_e32 v46, v6
	v_cvt_f32_f16_sdwa v55, v8 dst_sel:DWORD dst_unused:UNUSED_PAD src0_sel:WORD_1
	v_cvt_f32_f16_e32 v54, v8
	v_cvt_f32_f16_sdwa v57, v9 dst_sel:DWORD dst_unused:UNUSED_PAD src0_sel:WORD_1
	v_cvt_f32_f16_e32 v56, v9
	ds_read_b128 v[66:69], v137 offset:2048
	ds_read_b128 v[70:73], v137 offset:4096
	s_waitcnt lgkmcnt(0)
	v_mfma_f32_16x16x32_f16 v[42:45], v[50:53], v[58:61], v[44:47]
	v_cvt_f32_f16_sdwa v79, v12 dst_sel:DWORD dst_unused:UNUSED_PAD src0_sel:WORD_1
	v_cvt_f32_f16_e32 v78, v12
	v_cvt_f32_f16_sdwa v81, v13 dst_sel:DWORD dst_unused:UNUSED_PAD src0_sel:WORD_1
	s_mov_b32 m0, s88
	v_mfma_f32_16x16x32_f16 v[46:49], v[62:65], v[58:61], v[54:57]
	global_load_lds_dwordx4 v176, s[72:73]
	v_cvt_f32_f16_sdwa v59, v4 dst_sel:DWORD dst_unused:UNUSED_PAD src0_sel:WORD_1
	v_cvt_f32_f16_e32 v58, v4
	v_cvt_f32_f16_sdwa v61, v5 dst_sel:DWORD dst_unused:UNUSED_PAD src0_sel:WORD_1
	v_cvt_f32_f16_sdwa v55, v2 dst_sel:DWORD dst_unused:UNUSED_PAD src0_sel:WORD_1
	v_cvt_f32_f16_e32 v54, v2
	v_cvt_f32_f16_sdwa v57, v3 dst_sel:DWORD dst_unused:UNUSED_PAD src0_sel:WORD_1
	v_cvt_f32_f16_e32 v56, v3
	v_cvt_f32_f16_e32 v60, v5
	v_cvt_f32_f16_sdwa v3, v16 dst_sel:DWORD dst_unused:UNUSED_PAD src0_sel:WORD_1
	v_mfma_f32_16x16x32_f16 v[54:57], v[50:53], v[66:69], v[54:57]
	v_cvt_f32_f16_e32 v2, v16
	v_cvt_f32_f16_sdwa v5, v17 dst_sel:DWORD dst_unused:UNUSED_PAD src0_sel:WORD_1
	v_cvt_f32_f16_e32 v4, v17
	s_mov_b32 m0, s89
	v_mfma_f32_16x16x32_f16 v[58:61], v[62:65], v[66:69], v[58:61]
	global_load_lds_dwordx4 v177, s[72:73]
	v_cvt_f32_f16_sdwa v67, v14 dst_sel:DWORD dst_unused:UNUSED_PAD src0_sel:WORD_1
	v_cvt_f32_f16_e32 v66, v14
	v_cvt_f32_f16_sdwa v69, v7 dst_sel:DWORD dst_unused:UNUSED_PAD src0_sel:WORD_1
	v_cvt_f32_f16_e32 v68, v7
	ds_read_b128 v[6:9], v137 offset:6144
	v_cvt_f32_f16_e32 v80, v13
	v_mfma_f32_16x16x32_f16 v[66:69], v[50:53], v[70:73], v[66:69]
	v_cvt_f32_f16_sdwa v99, v28 dst_sel:DWORD dst_unused:UNUSED_PAD src0_sel:WORD_1
	v_cvt_f32_f16_e32 v98, v28
	v_cvt_f32_f16_sdwa v101, v29 dst_sel:DWORD dst_unused:UNUSED_PAD src0_sel:WORD_1
	s_mov_b32 m0, s90
	v_mfma_f32_16x16x32_f16 v[70:73], v[62:65], v[70:73], v[2:5]
	global_load_lds_dwordx4 v178, s[72:73]
	v_cvt_f32_f16_e32 v100, v29
	s_cmpk_gt_u32 s34, 0x8f
	s_cselect_b64 s[26:27], -1, 0
	v_cvt_f32_f16_sdwa v3, v10 dst_sel:DWORD dst_unused:UNUSED_PAD src0_sel:WORD_1
	v_cvt_f32_f16_e32 v2, v10
	v_cvt_f32_f16_sdwa v5, v11 dst_sel:DWORD dst_unused:UNUSED_PAD src0_sel:WORD_1
	v_cvt_f32_f16_e32 v4, v11
	ds_read_b128 v[10:13], v137 offset:8192
	s_waitcnt lgkmcnt(0)
	v_mfma_f32_16x16x32_f16 v[78:81], v[62:65], v[6:9], v[78:81]
	s_cmpk_lt_u32 s34, 0x90
	s_mov_b32 m0, s91
	v_mfma_f32_16x16x32_f16 v[74:77], v[50:53], v[6:9], v[2:5]
	global_load_lds_dwordx4 v179, s[72:73]
	v_cvt_f32_f16_sdwa v7, v22 dst_sel:DWORD dst_unused:UNUSED_PAD src0_sel:WORD_1
	v_cvt_f32_f16_e32 v6, v22
	v_cvt_f32_f16_sdwa v9, v15 dst_sel:DWORD dst_unused:UNUSED_PAD src0_sel:WORD_1
	v_cvt_f32_f16_sdwa v3, v24 dst_sel:DWORD dst_unused:UNUSED_PAD src0_sel:WORD_1
	v_cvt_f32_f16_e32 v2, v24
	v_cvt_f32_f16_sdwa v5, v25 dst_sel:DWORD dst_unused:UNUSED_PAD src0_sel:WORD_1
	v_cvt_f32_f16_e32 v4, v25
	v_cvt_f32_f16_e32 v8, v15
	ds_read_b128 v[14:17], v137 offset:10240
	v_mfma_f32_16x16x32_f16 v[22:25], v[62:65], v[10:13], v[2:5]
	s_nop 2
	v_cvt_f32_f16_sdwa v3, v18 dst_sel:DWORD dst_unused:UNUSED_PAD src0_sel:WORD_1
	v_cvt_f32_f16_e32 v2, v18
	v_cvt_f32_f16_sdwa v5, v19 dst_sel:DWORD dst_unused:UNUSED_PAD src0_sel:WORD_1
	v_cvt_f32_f16_e32 v4, v19
	s_mov_b32 m0, s92
	v_mfma_f32_16x16x32_f16 v[82:85], v[50:53], v[10:13], v[6:9]
	global_load_lds_dwordx4 v180, s[74:75]
	ds_read_b128 v[10:13], v137 offset:12288
	s_nop 1
	v_cvt_f32_f16_sdwa v7, v20 dst_sel:DWORD dst_unused:UNUSED_PAD src0_sel:WORD_1
	v_cvt_f32_f16_e32 v6, v20
	v_cvt_f32_f16_sdwa v9, v21 dst_sel:DWORD dst_unused:UNUSED_PAD src0_sel:WORD_1
	v_cvt_f32_f16_e32 v8, v21
	s_waitcnt lgkmcnt(0)
	v_mfma_f32_16x16x32_f16 v[86:89], v[50:53], v[14:17], v[2:5]
	s_nop 2
	v_cvt_f32_f16_sdwa v3, v32 dst_sel:DWORD dst_unused:UNUSED_PAD src0_sel:WORD_1
	v_cvt_f32_f16_e32 v2, v32
	v_cvt_f32_f16_sdwa v5, v33 dst_sel:DWORD dst_unused:UNUSED_PAD src0_sel:WORD_1
	v_cvt_f32_f16_e32 v4, v33
	s_mov_b32 m0, s93
	v_mfma_f32_16x16x32_f16 v[18:21], v[62:65], v[14:17], v[6:9]
	global_load_lds_dwordx4 v181, s[74:75]
	ds_read_b128 v[14:17], v137 offset:14336
	s_nop 1
	v_cvt_f32_f16_sdwa v7, v90 dst_sel:DWORD dst_unused:UNUSED_PAD src0_sel:WORD_1
	v_cvt_f32_f16_e32 v6, v90
	v_cvt_f32_f16_sdwa v9, v30 dst_sel:DWORD dst_unused:UNUSED_PAD src0_sel:WORD_1
	v_cvt_f32_f16_e32 v8, v30
	v_mfma_f32_16x16x32_f16 v[30:33], v[62:65], v[10:13], v[2:5]
	s_nop 2
	v_cvt_f32_f16_sdwa v3, v26 dst_sel:DWORD dst_unused:UNUSED_PAD src0_sel:WORD_1
	v_cvt_f32_f16_e32 v2, v26
	v_cvt_f32_f16_sdwa v5, v27 dst_sel:DWORD dst_unused:UNUSED_PAD src0_sel:WORD_1
	v_cvt_f32_f16_e32 v4, v27
	v_mfma_f32_16x16x32_f16 v[90:93], v[50:53], v[10:13], v[6:9]
	s_waitcnt lgkmcnt(0)
	v_mfma_f32_16x16x32_f16 v[94:97], v[50:53], v[14:17], v[2:5]
	s_nop 0
	v_cvt_f32_f16_sdwa v7, v38 dst_sel:DWORD dst_unused:UNUSED_PAD src0_sel:WORD_1
	v_cvt_f32_f16_e32 v6, v38
	v_cvt_f32_f16_sdwa v9, v39 dst_sel:DWORD dst_unused:UNUSED_PAD src0_sel:WORD_1
	v_cvt_f32_f16_sdwa v3, v40 dst_sel:DWORD dst_unused:UNUSED_PAD src0_sel:WORD_1
	v_cvt_f32_f16_e32 v2, v40
	v_cvt_f32_f16_sdwa v5, v41 dst_sel:DWORD dst_unused:UNUSED_PAD src0_sel:WORD_1
	v_cvt_f32_f16_e32 v4, v41
	v_cvt_f32_f16_e32 v8, v39
	v_mfma_f32_16x16x32_f16 v[98:101], v[62:65], v[14:17], v[98:101]
	s_cbranch_scc1 .LBB4_89
	ds_read_b128 v[10:13], v137 offset:16384
	s_waitcnt lgkmcnt(0)
	v_mfma_f32_16x16x32_f16 v[6:9], v[50:53], v[10:13], v[6:9]
	v_mfma_f32_16x16x32_f16 v[2:5], v[62:65], v[10:13], v[2:5]

.LBB4_96:
	v_add_u32_e32 v84, 0x5000, v135
	s_mov_b64 s[28:29], 0x180
	v_readfirstlane_b32 s34, v84
	v_add_u32_e32 v84, 0x7000, v135
	v_lshl_add_u64 v[82:83], v[116:117], 0, s[28:29]
	s_mov_b32 m0, s34
	v_readfirstlane_b32 s34, v84
	v_add_u32_e32 v84, 0x9000, v135
	s_barrier
	v_lshl_add_u64 v[82:83], v[114:115], 0, s[28:29]
	s_mov_b32 m0, s34
	v_readfirstlane_b32 s34, v84
	v_add_u32_e32 v84, 0xb000, v135
	v_lshl_add_u64 v[82:83], v[112:113], 0, s[28:29]
	s_mov_b32 m0, s34
	v_readfirstlane_b32 s34, v84
	v_lshl_add_u64 v[82:83], v[110:111], 0, s[28:29]
	s_mov_b32 m0, s34
	v_readfirstlane_b32 s34, v135
	v_add_u32_e32 v84, 0x2000, v135
	v_lshl_add_u64 v[82:83], v[120:121], 0, s[28:29]
	s_mov_b32 m0, s34
	v_readfirstlane_b32 s34, v84
	v_lshl_add_u64 v[82:83], v[118:119], 0, s[28:29]
	s_mov_b32 m0, s34
	s_and_b64 vcc, exec, s[14:15]
	s_cbranch_vccnz .LBB4_98
	v_add_u32_e32 v84, 0x4000, v135
	v_lshl_add_u64 v[82:83], v[122:123], 0, s[28:29]
	v_readfirstlane_b32 s28, v84
	s_mov_b32 m0, s28
	s_nop 0
	global_load_lds_dwordx4 v[82:83], off
.LBB4_98:
	s_add_u32 s72, s66, 0x180
	s_addc_u32 s73, s67, 0
	s_add_u32 s74, s68, 0x180
	s_addc_u32 s75, s69, 0
	v_add_u32_e32 v82, s36, v140
	v_add_u32_e32 v107, 0x5000, v82
	v_or_b32_e32 v106, v107, v141
	v_add_u32_e32 v142, 0, v106
	ds_read_b128 v[98:101], v142 offset:53248
	ds_read_b128 v[102:105], v142 offset:55296
	ds_read_b128 v[82:85], v137 offset:53248
	ds_read_b128 v[86:89], v137 offset:55296
	v_add_u32_e32 v140, 0xd000, v137
	s_and_b64 vcc, exec, s[24:25]
	s_waitcnt lgkmcnt(0)
	v_mfma_f32_16x16x32_f16 v[34:37], v[98:101], v[82:85], v[34:37]
	s_mov_b32 m0, s76
	v_mfma_f32_16x16x32_f16 v[38:41], v[102:105], v[82:85], v[38:41]
	global_load_lds_dwordx4 v176, s[72:73]
	v_mfma_f32_16x16x32_f16 v[42:45], v[98:101], v[86:89], v[42:45]
	s_mov_b32 m0, s77
	v_mfma_f32_16x16x32_f16 v[46:49], v[102:105], v[86:89], v[46:49]
	global_load_lds_dwordx4 v177, s[72:73]
	ds_read_b128 v[82:85], v137 offset:57344
	ds_read_b128 v[86:89], v137 offset:59392
	s_waitcnt lgkmcnt(0)
	v_mfma_f32_16x16x32_f16 v[50:53], v[98:101], v[82:85], v[50:53]
	s_mov_b32 m0, s78
	v_mfma_f32_16x16x32_f16 v[54:57], v[102:105], v[82:85], v[54:57]
	global_load_lds_dwordx4 v178, s[72:73]
	v_mfma_f32_16x16x32_f16 v[58:61], v[98:101], v[86:89], v[58:61]
	s_mov_b32 m0, s79
	v_mfma_f32_16x16x32_f16 v[62:65], v[102:105], v[86:89], v[62:65]
	global_load_lds_dwordx4 v179, s[72:73]
	ds_read_b128 v[82:85], v137 offset:61440
	ds_read_b128 v[86:89], v137 offset:63488
	s_waitcnt lgkmcnt(0)
	v_mfma_f32_16x16x32_f16 v[66:69], v[98:101], v[82:85], v[66:69]
	s_mov_b32 m0, s80
	v_mfma_f32_16x16x32_f16 v[70:73], v[102:105], v[82:85], v[70:73]
	global_load_lds_dwordx4 v180, s[74:75]
	v_mfma_f32_16x16x32_f16 v[82:85], v[102:105], v[86:89], v[18:21]
	s_nop 2
	ds_read_b128 v[18:21], v140 offset:12288
	ds_read_b128 v[148:151], v140 offset:14336
	s_mov_b32 m0, s81
	v_mfma_f32_16x16x32_f16 v[74:77], v[98:101], v[86:89], v[74:77]
	global_load_lds_dwordx4 v181, s[74:75]
	s_waitcnt lgkmcnt(0)
	v_mfma_f32_16x16x32_f16 v[86:89], v[98:101], v[18:21], v[22:25]
	v_mfma_f32_16x16x32_f16 v[90:93], v[102:105], v[18:21], v[26:29]
	v_mfma_f32_16x16x32_f16 v[94:97], v[98:101], v[148:151], v[30:33]
	v_mfma_f32_16x16x32_f16 v[78:81], v[102:105], v[148:151], v[78:81]
	s_cbranch_vccnz .LBB4_100
	ds_read_b128 v[18:21], v140 offset:16384
	s_waitcnt lgkmcnt(0)
	v_mfma_f32_16x16x32_f16 v[6:9], v[98:101], v[18:21], v[6:9]
	v_mfma_f32_16x16x32_f16 v[2:5], v[102:105], v[18:21], v[2:5]

.LBB4_107:
	s_mov_b64 s[28:29], 0x200
	v_readfirstlane_b32 s34, v136
	v_add_u32_e32 v174, 0x2000, v136
	v_lshl_add_u64 v[172:173], v[116:117], 0, s[28:29]
	s_mov_b32 m0, s34
	v_readfirstlane_b32 s34, v174
	v_add_u32_e32 v174, 0x4000, v136
	s_barrier
	s_waitcnt lgkmcnt(0)
	v_add_u32_e32 v90, s35, v106
	ds_read_b128 v[82:85], v90
	ds_read_b128 v[86:89], v90 offset:2048
	v_add_u32_e32 v146, s35, v146
	ds_read_b128 v[92:95], v146
	ds_read_b128 v[96:99], v146 offset:2048
	ds_read_b128 v[156:159], v146 offset:4096
	ds_read_b128 v[160:163], v146 offset:6144
	ds_read_b128 v[164:167], v146 offset:8192
	ds_read_b128 v[168:171], v146 offset:10240
	v_lshl_add_u64 v[172:173], v[114:115], 0, s[28:29]
	s_mov_b32 m0, s34
	v_readfirstlane_b32 s34, v174
	v_add_u32_e32 v174, 0x6000, v136
	v_lshl_add_u64 v[172:173], v[112:113], 0, s[28:29]
	s_mov_b32 m0, s34
	v_readfirstlane_b32 s34, v174
	v_add_u32_e32 v174, 0xd000, v135
	v_lshl_add_u64 v[172:173], v[110:111], 0, s[28:29]
	s_mov_b32 m0, s34
	v_readfirstlane_b32 s34, v174
	v_add_u32_e32 v174, 0xf000, v135
	v_lshl_add_u64 v[172:173], v[120:121], 0, s[28:29]
	s_mov_b32 m0, s34
	v_readfirstlane_b32 s34, v174
	v_lshl_add_u64 v[172:173], v[118:119], 0, s[28:29]
	s_mov_b32 m0, s34
	s_and_b64 vcc, exec, s[14:15]
	s_cbranch_vccnz .LBB4_109
	v_lshl_add_u64 v[172:173], v[122:123], 0, s[28:29]
	s_add_i32 s28, 0, 0x11000
	v_add_u32_e32 v174, s28, v1
	s_nop 0
	v_readfirstlane_b32 s28, v174
	s_mov_b32 m0, s28
	s_nop 0
	global_load_lds_dwordx4 v[172:173], off
.LBB4_109:
	s_add_u32 s72, s66, 0x200
	s_addc_u32 s73, s67, 0
	s_add_u32 s74, s68, 0x200
	s_addc_u32 s75, s69, 0
	s_and_b64 vcc, exec, s[24:25]
	s_waitcnt lgkmcnt(5)
	v_mfma_f32_16x16x32_f16 v[22:25], v[86:89], v[92:95], v[22:25]
	s_mov_b32 m0, s82
	v_mfma_f32_16x16x32_f16 v[18:21], v[82:85], v[92:95], v[18:21]
	global_load_lds_dwordx4 v176, s[72:73]
	s_waitcnt lgkmcnt(4)
	v_mfma_f32_16x16x32_f16 v[26:29], v[82:85], v[96:99], v[26:29]
	s_mov_b32 m0, s83
	v_mfma_f32_16x16x32_f16 v[30:33], v[86:89], v[96:99], v[30:33]
	global_load_lds_dwordx4 v177, s[72:73]
	s_waitcnt lgkmcnt(3)
	v_mfma_f32_16x16x32_f16 v[34:37], v[82:85], v[156:159], v[34:37]
	s_mov_b32 m0, s84
	v_mfma_f32_16x16x32_f16 v[38:41], v[86:89], v[156:159], v[38:41]
	global_load_lds_dwordx4 v178, s[72:73]
	ds_read_b128 v[156:159], v146 offset:12288
	s_waitcnt lgkmcnt(3)
	v_mfma_f32_16x16x32_f16 v[42:45], v[82:85], v[160:163], v[42:45]
	s_mov_b32 m0, s85
	v_mfma_f32_16x16x32_f16 v[46:49], v[86:89], v[160:163], v[46:49]
	global_load_lds_dwordx4 v179, s[72:73]
	ds_read_b128 v[160:163], v146 offset:14336
	s_waitcnt lgkmcnt(3)
	v_mfma_f32_16x16x32_f16 v[50:53], v[82:85], v[164:167], v[50:53]
	s_mov_b32 m0, s86
	v_mfma_f32_16x16x32_f16 v[54:57], v[86:89], v[164:167], v[54:57]
	global_load_lds_dwordx4 v180, s[74:75]
	s_waitcnt lgkmcnt(2)
	v_mfma_f32_16x16x32_f16 v[58:61], v[82:85], v[168:171], v[58:61]
	s_mov_b32 m0, s87
	v_mfma_f32_16x16x32_f16 v[62:65], v[86:89], v[168:171], v[62:65]
	global_load_lds_dwordx4 v181, s[74:75]
	s_waitcnt lgkmcnt(1)
	v_mfma_f32_16x16x32_f16 v[66:69], v[82:85], v[156:159], v[66:69]
	v_mfma_f32_16x16x32_f16 v[70:73], v[86:89], v[156:159], v[70:73]
	s_waitcnt lgkmcnt(0)
	v_mfma_f32_16x16x32_f16 v[74:77], v[82:85], v[160:163], v[74:77]
	v_mfma_f32_16x16x32_f16 v[78:81], v[86:89], v[160:163], v[78:81]
	s_cbranch_vccnz .LBB4_111
	ds_read_b128 v[92:95], v146 offset:16384
	s_waitcnt lgkmcnt(0)
	v_mfma_f32_16x16x32_f16 v[6:9], v[82:85], v[92:95], v[6:9]
	v_mfma_f32_16x16x32_f16 v[2:5], v[86:89], v[92:95], v[2:5]

.LBB4_121:
	s_mov_b64 s[30:31], 0x280
	v_readfirstlane_b32 s34, v144
	v_add_u32_e32 v174, 0x2000, v144
	v_lshl_add_u64 v[172:173], v[116:117], 0, s[30:31]
	s_mov_b32 m0, s34
	v_readfirstlane_b32 s34, v174
	v_add_u32_e32 v174, 0x4000, v144
	s_barrier
	s_waitcnt lgkmcnt(0)
	ds_read_b128 v[82:85], v138 offset:20480
	ds_read_b128 v[86:89], v138 offset:22528
	ds_read_b128 v[92:95], v137
	ds_read_b128 v[96:99], v137 offset:2048
	ds_read_b128 v[156:159], v137 offset:4096
	ds_read_b128 v[160:163], v137 offset:6144
	ds_read_b128 v[164:167], v137 offset:8192
	ds_read_b128 v[168:171], v137 offset:10240
	v_lshl_add_u64 v[172:173], v[114:115], 0, s[30:31]
	s_mov_b32 m0, s34
	v_readfirstlane_b32 s34, v174
	v_add_u32_e32 v174, 0x6000, v144
	v_lshl_add_u64 v[172:173], v[112:113], 0, s[30:31]
	s_mov_b32 m0, s34
	v_readfirstlane_b32 s34, v174
	v_lshl_add_u64 v[172:173], v[110:111], 0, s[30:31]
	s_mov_b32 m0, s34
	v_readfirstlane_b32 s34, v145
	v_add_u32_e32 v174, 0x2000, v145
	v_lshl_add_u64 v[172:173], v[120:121], 0, s[30:31]
	s_mov_b32 m0, s34
	v_readfirstlane_b32 s34, v174
	v_lshl_add_u64 v[172:173], v[118:119], 0, s[30:31]
	s_mov_b32 m0, s34
	s_and_b64 vcc, exec, s[14:15]
	s_cbranch_vccnz .LBB4_123
	v_lshl_add_u64 v[172:173], v[122:123], 0, s[30:31]
	s_add_i32 s30, 0, 0x1e000
	v_add_u32_e32 v174, s30, v1
	s_nop 0
	v_readfirstlane_b32 s30, v174
	s_mov_b32 m0, s30
	s_nop 0
	global_load_lds_dwordx4 v[172:173], off
.LBB4_123:
	s_add_u32 s72, s66, 0x280
	s_addc_u32 s73, s67, 0
	s_add_u32 s74, s68, 0x280
	s_addc_u32 s75, s69, 0
	s_and_b64 vcc, exec, s[24:25]
	s_waitcnt lgkmcnt(5)
	v_mfma_f32_16x16x32_f16 v[18:21], v[82:85], v[92:95], v[18:21]
	s_mov_b32 m0, s88
	v_mfma_f32_16x16x32_f16 v[22:25], v[86:89], v[92:95], v[22:25]
	global_load_lds_dwordx4 v176, s[72:73]
	s_waitcnt lgkmcnt(4)
	v_mfma_f32_16x16x32_f16 v[26:29], v[82:85], v[96:99], v[26:29]
	s_mov_b32 m0, s89
	v_mfma_f32_16x16x32_f16 v[30:33], v[86:89], v[96:99], v[30:33]
	global_load_lds_dwordx4 v177, s[72:73]
	s_waitcnt lgkmcnt(3)
	v_mfma_f32_16x16x32_f16 v[34:37], v[82:85], v[156:159], v[34:37]
	s_mov_b32 m0, s90
	v_mfma_f32_16x16x32_f16 v[38:41], v[86:89], v[156:159], v[38:41]
	global_load_lds_dwordx4 v178, s[72:73]
	ds_read_b128 v[156:159], v137 offset:12288
	s_waitcnt lgkmcnt(3)
	v_mfma_f32_16x16x32_f16 v[42:45], v[82:85], v[160:163], v[42:45]
	s_mov_b32 m0, s91
	v_mfma_f32_16x16x32_f16 v[46:49], v[86:89], v[160:163], v[46:49]
	global_load_lds_dwordx4 v179, s[72:73]
	ds_read_b128 v[160:163], v137 offset:14336
	s_waitcnt lgkmcnt(3)
	v_mfma_f32_16x16x32_f16 v[50:53], v[82:85], v[164:167], v[50:53]
	s_mov_b32 m0, s92
	v_mfma_f32_16x16x32_f16 v[54:57], v[86:89], v[164:167], v[54:57]
	global_load_lds_dwordx4 v180, s[74:75]
	s_waitcnt lgkmcnt(2)
	v_mfma_f32_16x16x32_f16 v[58:61], v[82:85], v[168:171], v[58:61]
	s_mov_b32 m0, s93
	v_mfma_f32_16x16x32_f16 v[62:65], v[86:89], v[168:171], v[62:65]
	global_load_lds_dwordx4 v181, s[74:75]
	s_waitcnt lgkmcnt(1)
	v_mfma_f32_16x16x32_f16 v[66:69], v[82:85], v[156:159], v[66:69]
	v_mfma_f32_16x16x32_f16 v[70:73], v[86:89], v[156:159], v[70:73]
	s_waitcnt lgkmcnt(0)
	v_mfma_f32_16x16x32_f16 v[74:77], v[82:85], v[160:163], v[74:77]
	v_mfma_f32_16x16x32_f16 v[78:81], v[86:89], v[160:163], v[78:81]
	s_cbranch_vccnz .LBB4_125
	ds_read_b128 v[92:95], v137 offset:16384
	s_waitcnt lgkmcnt(0)
	v_mfma_f32_16x16x32_f16 v[6:9], v[82:85], v[92:95], v[6:9]
	v_mfma_f32_16x16x32_f16 v[2:5], v[86:89], v[92:95], v[2:5]

.LBB4_132:
	v_add_u32_e32 v174, 0x5000, v135
	s_mov_b64 s[30:31], 0x300
	v_readfirstlane_b32 s34, v174
	v_add_u32_e32 v174, 0x7000, v135
	v_lshl_add_u64 v[172:173], v[116:117], 0, s[30:31]
	s_mov_b32 m0, s34
	v_readfirstlane_b32 s34, v174
	v_add_u32_e32 v174, 0x9000, v135
	s_barrier
	s_waitcnt lgkmcnt(0)
	ds_read_b128 v[82:85], v142 offset:53248
	ds_read_b128 v[86:89], v142 offset:55296
	ds_read_b128 v[92:95], v137 offset:53248
	ds_read_b128 v[96:99], v137 offset:55296
	ds_read_b128 v[156:159], v137 offset:57344
	ds_read_b128 v[160:163], v137 offset:59392
	ds_read_b128 v[164:167], v137 offset:61440
	ds_read_b128 v[168:171], v137 offset:63488
	v_lshl_add_u64 v[172:173], v[114:115], 0, s[30:31]
	s_mov_b32 m0, s34
	v_readfirstlane_b32 s34, v174
	v_add_u32_e32 v174, 0xb000, v135
	v_lshl_add_u64 v[172:173], v[112:113], 0, s[30:31]
	s_mov_b32 m0, s34
	v_readfirstlane_b32 s34, v174
	v_lshl_add_u64 v[172:173], v[110:111], 0, s[30:31]
	s_mov_b32 m0, s34
	v_readfirstlane_b32 s34, v135
	v_add_u32_e32 v174, 0x2000, v135
	v_lshl_add_u64 v[172:173], v[120:121], 0, s[30:31]
	s_mov_b32 m0, s34
	v_readfirstlane_b32 s34, v174
	v_lshl_add_u64 v[172:173], v[118:119], 0, s[30:31]
	s_mov_b32 m0, s34
	s_and_b64 vcc, exec, s[14:15]
	s_cbranch_vccnz .LBB4_134
	v_add_u32_e32 v174, 0x4000, v135
	v_lshl_add_u64 v[172:173], v[122:123], 0, s[30:31]
	v_readfirstlane_b32 s30, v174
	s_mov_b32 m0, s30
	s_nop 0
	global_load_lds_dwordx4 v[172:173], off
.LBB4_134:
	s_add_u32 s72, s66, 0x300
	s_addc_u32 s73, s67, 0
	s_add_u32 s74, s68, 0x300
	s_addc_u32 s75, s69, 0
	s_and_b64 vcc, exec, s[24:25]
	s_waitcnt lgkmcnt(5)
	v_mfma_f32_16x16x32_f16 v[18:21], v[82:85], v[92:95], v[18:21]
	s_mov_b32 m0, s76
	v_mfma_f32_16x16x32_f16 v[22:25], v[86:89], v[92:95], v[22:25]
	global_load_lds_dwordx4 v176, s[72:73]
	s_waitcnt lgkmcnt(4)
	v_mfma_f32_16x16x32_f16 v[26:29], v[82:85], v[96:99], v[26:29]
	s_mov_b32 m0, s77
	v_mfma_f32_16x16x32_f16 v[30:33], v[86:89], v[96:99], v[30:33]
	global_load_lds_dwordx4 v177, s[72:73]
	s_waitcnt lgkmcnt(3)
	v_mfma_f32_16x16x32_f16 v[34:37], v[82:85], v[156:159], v[34:37]
	s_mov_b32 m0, s78
	v_mfma_f32_16x16x32_f16 v[38:41], v[86:89], v[156:159], v[38:41]
	global_load_lds_dwordx4 v178, s[72:73]
	ds_read_b128 v[156:159], v140 offset:12288
	s_waitcnt lgkmcnt(3)
	v_mfma_f32_16x16x32_f16 v[42:45], v[82:85], v[160:163], v[42:45]
	s_mov_b32 m0, s79
	v_mfma_f32_16x16x32_f16 v[46:49], v[86:89], v[160:163], v[46:49]
	global_load_lds_dwordx4 v179, s[72:73]
	ds_read_b128 v[160:163], v140 offset:14336
	s_waitcnt lgkmcnt(3)
	v_mfma_f32_16x16x32_f16 v[50:53], v[82:85], v[164:167], v[50:53]
	s_mov_b32 m0, s80
	v_mfma_f32_16x16x32_f16 v[54:57], v[86:89], v[164:167], v[54:57]
	global_load_lds_dwordx4 v180, s[74:75]
	s_waitcnt lgkmcnt(2)
	v_mfma_f32_16x16x32_f16 v[58:61], v[82:85], v[168:171], v[58:61]
	s_mov_b32 m0, s81
	v_mfma_f32_16x16x32_f16 v[62:65], v[86:89], v[168:171], v[62:65]
	global_load_lds_dwordx4 v181, s[74:75]
	s_waitcnt lgkmcnt(1)
	v_mfma_f32_16x16x32_f16 v[66:69], v[82:85], v[156:159], v[66:69]
	v_mfma_f32_16x16x32_f16 v[70:73], v[86:89], v[156:159], v[70:73]
	s_waitcnt lgkmcnt(0)
	v_mfma_f32_16x16x32_f16 v[74:77], v[82:85], v[160:163], v[74:77]
	v_mfma_f32_16x16x32_f16 v[78:81], v[86:89], v[160:163], v[78:81]
	s_cbranch_vccnz .LBB4_136
	ds_read_b128 v[92:95], v140 offset:16384
	s_waitcnt lgkmcnt(0)
	v_mfma_f32_16x16x32_f16 v[6:9], v[82:85], v[92:95], v[6:9]
	v_mfma_f32_16x16x32_f16 v[2:5], v[86:89], v[92:95], v[2:5]

.LBB4_143:
	s_mov_b64 s[30:31], 0x380
	v_readfirstlane_b32 s34, v136
	v_add_u32_e32 v84, 0x2000, v136
	v_lshl_add_u64 v[82:83], v[116:117], 0, s[30:31]
	s_mov_b32 m0, s34
	v_readfirstlane_b32 s34, v84
	v_add_u32_e32 v84, 0x4000, v136
	s_barrier
	v_lshl_add_u64 v[82:83], v[114:115], 0, s[30:31]
	s_mov_b32 m0, s34
	v_readfirstlane_b32 s34, v84
	v_add_u32_e32 v84, 0x6000, v136
	v_lshl_add_u64 v[82:83], v[112:113], 0, s[30:31]
	s_mov_b32 m0, s34
	v_readfirstlane_b32 s34, v84
	v_add_u32_e32 v84, 0xd000, v135
	v_lshl_add_u64 v[82:83], v[110:111], 0, s[30:31]
	s_mov_b32 m0, s34
	v_readfirstlane_b32 s34, v84
	v_add_u32_e32 v84, 0xf000, v135
	v_lshl_add_u64 v[82:83], v[120:121], 0, s[30:31]
	s_mov_b32 m0, s34
	v_readfirstlane_b32 s34, v84
	v_lshl_add_u64 v[82:83], v[118:119], 0, s[30:31]
	s_mov_b32 m0, s34
	s_and_b64 vcc, exec, s[14:15]
	s_cbranch_vccnz .LBB4_145
	s_add_i32 s14, 0, 0x11000
	v_add_u32_e32 v1, s14, v1
	v_lshl_add_u64 v[82:83], v[122:123], 0, s[30:31]
	v_readfirstlane_b32 s14, v1
	s_mov_b32 m0, s14
	s_nop 0
	global_load_lds_dwordx4 v[82:83], off
.LBB4_145:
	s_add_u32 s72, s66, 0x380
	s_addc_u32 s73, s67, 0
	s_add_u32 s74, s68, 0x380
	s_addc_u32 s75, s69, 0
	s_waitcnt lgkmcnt(0)
	ds_read_b128 v[114:117], v90
	ds_read_b128 v[118:121], v90 offset:2048
	ds_read_b128 v[82:85], v146
	ds_read_b128 v[86:89], v146 offset:2048
	ds_read_b128 v[156:159], v146 offset:4096
	ds_read_b128 v[160:163], v146 offset:6144
	ds_read_b128 v[164:167], v146 offset:8192
	ds_read_b128 v[168:171], v146 offset:10240
	s_and_b64 vcc, exec, s[24:25]
	s_waitcnt lgkmcnt(5)
	v_mfma_f32_16x16x32_f16 v[18:21], v[114:117], v[82:85], v[18:21]
	s_mov_b32 m0, s82
	v_mfma_f32_16x16x32_f16 v[22:25], v[118:121], v[82:85], v[22:25]
	global_load_lds_dwordx4 v176, s[72:73]
	s_waitcnt lgkmcnt(4)
	v_mfma_f32_16x16x32_f16 v[26:29], v[114:117], v[86:89], v[26:29]
	s_mov_b32 m0, s83
	v_mfma_f32_16x16x32_f16 v[30:33], v[118:121], v[86:89], v[30:33]
	global_load_lds_dwordx4 v177, s[72:73]
	s_waitcnt lgkmcnt(2)
	v_mfma_f32_16x16x32_f16 v[42:45], v[114:117], v[160:163], v[42:45]
	s_mov_b32 m0, s84
	v_mfma_f32_16x16x32_f16 v[46:49], v[118:121], v[160:163], v[46:49]
	global_load_lds_dwordx4 v178, s[72:73]
	v_mfma_f32_16x16x32_f16 v[34:37], v[114:117], v[156:159], v[34:37]
	s_mov_b32 m0, s85
	v_mfma_f32_16x16x32_f16 v[38:41], v[118:121], v[156:159], v[38:41]
	global_load_lds_dwordx4 v179, s[72:73]
	ds_read_b128 v[156:159], v146 offset:12288
	ds_read_b128 v[160:163], v146 offset:14336
	s_waitcnt lgkmcnt(3)
	v_mfma_f32_16x16x32_f16 v[82:85], v[114:117], v[164:167], v[50:53]
	s_mov_b32 m0, s86
	v_mfma_f32_16x16x32_f16 v[86:89], v[118:121], v[164:167], v[54:57]
	global_load_lds_dwordx4 v180, s[74:75]
	s_nop 1
	s_waitcnt lgkmcnt(2)
	v_mfma_f32_16x16x32_f16 v[90:93], v[114:117], v[168:171], v[58:61]
	s_mov_b32 m0, s87
	v_mfma_f32_16x16x32_f16 v[94:97], v[118:121], v[168:171], v[62:65]
	global_load_lds_dwordx4 v181, s[74:75]
	s_waitcnt lgkmcnt(1)
	v_mfma_f32_16x16x32_f16 v[98:101], v[114:117], v[156:159], v[66:69]
	v_mfma_f32_16x16x32_f16 v[102:105], v[118:121], v[156:159], v[70:73]
	s_waitcnt lgkmcnt(0)
	v_mfma_f32_16x16x32_f16 v[106:109], v[114:117], v[160:163], v[74:77]
	v_mfma_f32_16x16x32_f16 v[110:113], v[118:121], v[160:163], v[78:81]
	s_cbranch_vccnz .LBB4_147
	ds_read_b128 v[50:53], v146 offset:16384
	s_waitcnt lgkmcnt(0)
	v_mfma_f32_16x16x32_f16 v[6:9], v[114:117], v[50:53], v[6:9]
	v_mfma_f32_16x16x32_f16 v[2:5], v[118:121], v[50:53], v[2:5]

	.amdhsa_kernel _Z8moe_gemmILi2EEvPKDF16_S1_PvPKyPKiPKfS1_
		.amdhsa_group_segment_fixed_size 0
		.amdhsa_private_segment_fixed_size 0
		.amdhsa_kernarg_size 56
		.amdhsa_user_sgpr_count 2
		.amdhsa_user_sgpr_dispatch_ptr 0
		.amdhsa_user_sgpr_queue_ptr 0
		.amdhsa_user_sgpr_kernarg_segment_ptr 1
		.amdhsa_user_sgpr_dispatch_id 0
		.amdhsa_user_sgpr_kernarg_preload_length 0
		.amdhsa_user_sgpr_kernarg_preload_offset 0
		.amdhsa_user_sgpr_private_segment_size 0
		.amdhsa_uses_dynamic_stack 0
		.amdhsa_enable_private_segment 0
		.amdhsa_system_sgpr_workgroup_id_x 1
		.amdhsa_system_sgpr_workgroup_id_y 0
		.amdhsa_system_sgpr_workgroup_id_z 0
		.amdhsa_system_sgpr_workgroup_info 0
		.amdhsa_system_vgpr_workitem_id 0
		.amdhsa_next_free_vgpr 184
		.amdhsa_next_free_sgpr 94
		.amdhsa_accum_offset 184
		.amdhsa_reserve_vcc 1
		.amdhsa_float_round_mode_32 0
		.amdhsa_float_round_mode_16_64 0
		.amdhsa_float_denorm_mode_32 3
		.amdhsa_float_denorm_mode_16_64 3
		.amdhsa_dx10_clamp 1
		.amdhsa_ieee_mode 1
		.amdhsa_fp16_overflow 0
		.amdhsa_tg_split 0
		.amdhsa_exception_fp_ieee_invalid_op 0
		.amdhsa_exception_fp_denorm_src 0
		.amdhsa_exception_fp_ieee_div_zero 0
		.amdhsa_exception_fp_ieee_overflow 0
		.amdhsa_exception_fp_ieee_underflow 0
		.amdhsa_exception_fp_ieee_inexact 0
		.amdhsa_exception_int_div_zero 0
	.end_amdhsa_kernel

amdhsa.kernels:
  - .agpr_count:     0
    .args:
      - .actual_access:  write_only
        .address_space:  global
        .offset:         0
        .size:           8
        .value_kind:     global_buffer
    .group_segment_fixed_size: 0
    .kernarg_segment_align: 8
    .kernarg_segment_size: 8
    .language:       OpenCL C
    .language_version:
      - 2
      - 0
    .max_flat_workgroup_size: 1024
    .name:           _Z15zero_cnt_kernelPy
    .private_segment_fixed_size: 0
    .sgpr_count:     10
    .sgpr_spill_count: 0
    .symbol:         _Z15zero_cnt_kernelPy.kd
    .uniform_work_group_size: 1
    .uses_dynamic_stack: false
    .vgpr_count:     3
    .vgpr_spill_count: 0
    .wavefront_size: 64
  - .agpr_count:     0
    .args:
      - .actual_access:  read_only
        .address_space:  global
        .offset:         0
        .size:           8
        .value_kind:     global_buffer
      - .actual_access:  read_only
        .address_space:  global
        .offset:         8
        .size:           8
        .value_kind:     global_buffer
      - .actual_access:  read_only
        .address_space:  global
        .offset:         16
        .size:           8
        .value_kind:     global_buffer
      - .actual_access:  read_only
        .address_space:  global
        .offset:         24
        .size:           8
        .value_kind:     global_buffer
      - .actual_access:  write_only
        .address_space:  global
        .offset:         32
        .size:           8
        .value_kind:     global_buffer
      - .actual_access:  write_only
        .address_space:  global
        .offset:         40
        .size:           8
        .value_kind:     global_buffer
      - .actual_access:  write_only
        .address_space:  global
        .offset:         48
        .size:           8
        .value_kind:     global_buffer
      - .address_space:  global
        .offset:         56
        .size:           8
        .value_kind:     global_buffer
      - .actual_access:  write_only
        .address_space:  global
        .offset:         64
        .size:           8
        .value_kind:     global_buffer
      - .actual_access:  write_only
        .address_space:  global
        .offset:         72
        .size:           8
        .value_kind:     global_buffer
    .group_segment_fixed_size: 0
    .kernarg_segment_align: 8
    .kernarg_segment_size: 80
    .language:       OpenCL C
    .language_version:
      - 2
      - 0
    .max_flat_workgroup_size: 256
    .name:           _Z11prep_kernelPKfS0_S0_S0_PDF16_S1_S1_PyPiPf
    .private_segment_fixed_size: 0
    .sgpr_count:     55
    .sgpr_spill_count: 0
    .symbol:         _Z11prep_kernelPKfS0_S0_S0_PDF16_S1_S1_PyPiPf.kd
    .uniform_work_group_size: 1
    .uses_dynamic_stack: false
    .vgpr_count:     248
    .vgpr_spill_count: 0
    .wavefront_size: 64
  - .agpr_count:     0
    .args:
      - .address_space:  global
        .offset:         0
        .size:           8
        .value_kind:     global_buffer
      - .address_space:  global
        .offset:         8
        .size:           8
        .value_kind:     global_buffer
      - .actual_access:  write_only
        .address_space:  global
        .offset:         16
        .size:           8
        .value_kind:     global_buffer
      - .actual_access:  read_only
        .address_space:  global
        .offset:         24
        .size:           8
        .value_kind:     global_buffer
      - .actual_access:  read_only
        .address_space:  global
        .offset:         32
        .size:           8
        .value_kind:     global_buffer
      - .actual_access:  read_only
        .address_space:  global
        .offset:         40
        .size:           8
        .value_kind:     global_buffer
      - .actual_access:  read_only
        .address_space:  global
        .offset:         48
        .size:           8
        .value_kind:     global_buffer
    .group_segment_fixed_size: 0
    .kernarg_segment_align: 8
    .kernarg_segment_size: 56
    .language:       OpenCL C
    .language_version:
      - 2
      - 0
    .max_flat_workgroup_size: 512
    .name:           _Z8moe_gemmILi0EEvPKDF16_S1_PvPKyPKiPKfS1_
    .private_segment_fixed_size: 0
    .sgpr_count:     98
    .sgpr_spill_count: 0
    .symbol:         _Z8moe_gemmILi0EEvPKDF16_S1_PvPKyPKiPKfS1_.kd
    .uniform_work_group_size: 1
    .uses_dynamic_stack: false
    .vgpr_count:     256
    .vgpr_spill_count: 0
    .wavefront_size: 64
  - .agpr_count:     0
    .args:
      - .address_space:  global
        .offset:         0
        .size:           8
        .value_kind:     global_buffer
      - .address_space:  global
        .offset:         8
        .size:           8
        .value_kind:     global_buffer
      - .actual_access:  write_only
        .address_space:  global
        .offset:         16
        .size:           8
        .value_kind:     global_buffer
      - .actual_access:  read_only
        .address_space:  global
        .offset:         24
        .size:           8
        .value_kind:     global_buffer
      - .actual_access:  read_only
        .address_space:  global
        .offset:         32
        .size:           8
        .value_kind:     global_buffer
      - .actual_access:  read_only
        .address_space:  global
        .offset:         40
        .size:           8
        .value_kind:     global_buffer
      - .actual_access:  read_only
        .address_space:  global
        .offset:         48
        .size:           8
        .value_kind:     global_buffer
    .group_segment_fixed_size: 0
    .kernarg_segment_align: 8
    .kernarg_segment_size: 56
    .language:       OpenCL C
    .language_version:
      - 2
      - 0
    .max_flat_workgroup_size: 512
    .name:           _Z8moe_gemmILi1EEvPKDF16_S1_PvPKyPKiPKfS1_
    .private_segment_fixed_size: 0
    .sgpr_count:     100
    .sgpr_spill_count: 0
    .symbol:         _Z8moe_gemmILi1EEvPKDF16_S1_PvPKyPKiPKfS1_.kd
    .uniform_work_group_size: 1
    .uses_dynamic_stack: false
    .vgpr_count:     176
    .vgpr_spill_count: 0
    .wavefront_size: 64
  - .agpr_count:     0
    .args:
      - .address_space:  global
        .offset:         0
        .size:           8
        .value_kind:     global_buffer
      - .address_space:  global
        .offset:         8
        .size:           8
        .value_kind:     global_buffer
      - .actual_access:  write_only
        .address_space:  global
        .offset:         16
        .size:           8
        .value_kind:     global_buffer
      - .actual_access:  read_only
        .address_space:  global
        .offset:         24
        .size:           8
        .value_kind:     global_buffer
      - .actual_access:  read_only
        .address_space:  global
        .offset:         32
        .size:           8
        .value_kind:     global_buffer
      - .actual_access:  read_only
        .address_space:  global
        .offset:         40
        .size:           8
        .value_kind:     global_buffer
      - .actual_access:  read_only
        .address_space:  global
        .offset:         48
        .size:           8
        .value_kind:     global_buffer
    .group_segment_fixed_size: 0
    .kernarg_segment_align: 8
    .kernarg_segment_size: 56
    .language:       OpenCL C
    .language_version:
      - 2
      - 0
    .max_flat_workgroup_size: 512
    .name:           _Z8moe_gemmILi2EEvPKDF16_S1_PvPKyPKiPKfS1_
    .private_segment_fixed_size: 0
    .sgpr_count:     100
    .sgpr_spill_count: 0
    .symbol:         _Z8moe_gemmILi2EEvPKDF16_S1_PvPKyPKiPKfS1_.kd
    .uniform_work_group_size: 1
    .uses_dynamic_stack: false
    .vgpr_count:     184
    .vgpr_spill_count: 0
    .wavefront_size: 64
